# speedup vs baseline: 1.0040x; 1.0040x over previous
_Z7k_layerILi1EEvPKDF16_S1_PKfS3_S3_S3_S3_S3_S1_S1_S1_S1_S3_S3_PKhS5_PDF16_S6_PfS7_:
	s_ashr_i32 s3, s2, 1
	s_and_b32 s3, s3, -8
	s_and_b32 s16, s2, 7
	v_readfirstlane_b32 s15, v0
	s_or_b32 s12, s3, s16
	s_bfe_u32 s14, s2, 0x10003
	s_cmpk_gt_u32 s15, 0xff
	s_mov_b64 s[2:3], -1
	s_cbranch_scc0 .LBB2_17
	s_mov_b32 s44, 0x3e000000
	v_mov_b32_e32 v240, 0x64646464
	s_mov_b32 s42, 0x4010400
	s_mov_b32 s43, 0x4030402
	s_load_dwordx2 s[4:5], s[0:1], 0x80
	s_load_dwordx2 s[8:9], s[0:1], 0x0
	v_lshlrev_b32_e32 v2, 3, v0
	v_add_u32_e32 v1, 0xffffff00, v0
	v_ashrrev_i32_e32 v3, 4, v1
	v_and_b32_e32 v38, 0x78, v2
	s_lshl_b32 s17, s12, 9
	v_add_u32_e32 v2, s17, v3
	v_lshlrev_b32_e32 v4, 1, v38
	s_mov_b32 s7, 0x20000
	s_mov_b32 s6, 0x1000000
	v_lshl_or_b32 v2, v2, 8, v4
	s_waitcnt lgkmcnt(0)
	s_and_b32 s9, s9, 0xffff
	s_mov_b32 s10, s6
	s_mov_b32 s11, s7
	v_add_u32_e32 v5, 0x4000, v2
	buffer_load_dwordx4 v[10:13], v2, s[8:11], 0 offen sc1
	buffer_load_dwordx4 v[18:21], v5, s[8:11], 0 offen sc1
	v_add_u32_e32 v5, 0x1000, v2
	buffer_load_dwordx4 v[26:29], v5, s[8:11], 0 offen sc1
	v_add_u32_e32 v5, 0x2000, v2
	v_add_u32_e32 v6, 0x3000, v2
	buffer_load_dwordx4 v[30:33], v5, s[8:11], 0 offen sc1
	buffer_load_dwordx4 v[58:61], v6, s[8:11], 0 offen sc1
	v_add_u32_e32 v5, 0x5000, v2
	buffer_load_dwordx4 v[34:37], v5, s[8:11], 0 offen sc1
	v_add_u32_e32 v5, 0x6000, v2
	v_add_u32_e32 v2, 0x7000, v2
	buffer_load_dwordx4 v[62:65], v5, s[8:11], 0 offen sc1
	buffer_load_dwordx4 v[66:69], v2, s[8:11], 0 offen sc1
	s_or_b32 s2, s17, 0x80
	v_add_u32_e32 v2, s2, v3
	v_lshl_or_b32 v6, v2, 8, v4
	v_add_u32_e32 v2, 0x1000, v6
	v_add_u32_e32 v7, 0x2000, v6
	v_add_u32_e32 v8, 0x3000, v6
	buffer_load_dwordx4 v[70:73], v6, s[8:11], 0 offen sc1
	buffer_load_dwordx4 v[74:77], v2, s[8:11], 0 offen sc1
	buffer_load_dwordx4 v[14:17], v7, s[8:11], 0 offen sc1
	s_nop 0
	buffer_load_dwordx4 v[2:5], v8, s[8:11], 0 offen sc1
	v_add_u32_e32 v7, 0x4000, v6
	v_add_u32_e32 v8, 0x5000, v6
	v_add_u32_e32 v39, 0x6000, v6
	buffer_load_dwordx4 v[78:81], v7, s[8:11], 0 offen sc1
	buffer_load_dwordx4 v[82:85], v8, s[8:11], 0 offen sc1
	v_add_u32_e32 v40, 0x7000, v6
	buffer_load_dwordx4 v[22:25], v39, s[8:11], 0 offen sc1
	buffer_load_dwordx4 v[6:9], v40, s[8:11], 0 offen sc1
	v_lshlrev_b32_e32 v48, 2, v38
	v_or_b32_e32 v38, 0x1e600, v48
	s_barrier
	ds_read_b128 v[38:41], v38
	v_or_b32_e32 v42, 0x1ea00, v48
	ds_read_b128 v[42:45], v42
	v_or_b32_e32 v49, 0x1e800, v48
	v_or_b32_e32 v50, 0x1ec00, v48
	s_waitcnt lgkmcnt(1)
	v_cvt_pk_f16_f32 v46, v38, v39
	v_or_b32_e32 v38, 0x1e610, v48
	v_cvt_pk_f16_f32 v47, v40, v41
	ds_read_b128 v[38:41], v38
	v_or_b32_e32 v51, 0x1ea10, v48
	ds_read_b128 v[54:57], v49
	ds_read_b128 v[86:89], v50
	ds_read_b128 v[90:93], v51
	v_or_b32_e32 v94, 0x1e810, v48
	v_or_b32_e32 v48, 0x1ec10, v48
	s_waitcnt lgkmcnt(3)
	v_cvt_pk_f16_f32 v51, v38, v39
	s_waitcnt lgkmcnt(2)
	v_pk_fma_f32 v[38:39], v[54:55], 0, v[42:43] op_sel_hi:[1,0,1]
	v_cvt_pk_f16_f32 v52, v40, v41
	s_waitcnt lgkmcnt(1)
	v_pk_add_f32 v[38:39], v[86:87], v[38:39]
	v_pk_fma_f32 v[42:43], v[56:57], 0, v[44:45] op_sel_hi:[1,0,1]
	v_cvt_pk_f16_f32 v53, v38, v39
	ds_read_b128 v[38:41], v94
	ds_read_b128 v[94:97], v48
	v_pk_add_f32 v[42:43], v[88:89], v[42:43]
	s_movk_i32 s13, 0x110
	v_cvt_pk_f16_f32 v55, v42, v43
	s_waitcnt lgkmcnt(1)
	v_pk_fma_f32 v[38:39], v[38:39], 0, v[90:91] op_sel_hi:[1,0,1]
	s_or_b32 s20, s17, 0x100
	s_waitcnt lgkmcnt(0)
	v_pk_add_f32 v[38:39], v[94:95], v[38:39]
	s_or_b32 s18, s17, 0x180
	v_cvt_pk_f16_f32 v56, v38, v39
	v_pk_fma_f32 v[38:39], v[40:41], 0, v[92:93] op_sel_hi:[1,0,1]
	s_lshl_b32 s17, s14, 6
	v_pk_add_f32 v[38:39], v[96:97], v[38:39]
	v_mov_b32_e32 v122, 0x11000
	v_cvt_pk_f16_f32 v57, v38, v39
	v_mov_b32_e32 v38, v0
	s_and_b32 s5, s5, 0xffff
	v_add_u32_e32 v39, 0xffffff00, v38
	v_lshlrev_b32_e32 v38, 4, v38
	v_ashrrev_i32_e32 v39, 4, v39
	v_and_b32_e32 v40, 0xf0, v38
	v_mad_u64_u32 v[42:43], s[22:23], v39, s13, v[40:41]
	s_lshl_b32 s2, s2, 7
	s_or_b32 s2, s2, s17
	s_mov_b32 s3, 0
	s_lshr_b32 s19, s15, 6
	s_movk_i32 s21, 0x1000
	s_waitcnt vmcnt(15)
	v_pk_fma_f16 v12, v51, v12, v56
	v_pk_fma_f16 v10, v46, v10, v53
	v_pk_fma_f16 v13, v52, v13, v57
	v_pk_fma_f16 v11, v47, v11, v55
	s_waitcnt vmcnt(14)
	v_pk_fma_f16 v20, v51, v20, v56
	v_pk_fma_f16 v18, v46, v18, v53
	v_pk_fma_f16 v21, v52, v21, v57
	v_pk_fma_f16 v19, v47, v19, v55
	ds_write_b128 v42, v[10:13]
	ds_write_b128 v42, v[18:21] offset:17408
	v_pk_add_f16 v44, v13, v21
	v_pk_add_f16 v48, v12, v20
	v_pk_add_f16 v54, v11, v19
	v_pk_add_f16 v114, v10, v18
	s_waitcnt vmcnt(13)
	v_pk_fma_f16 v12, v51, v28, v56
	v_pk_fma_f16 v10, v46, v26, v53
	v_pk_fma_f16 v13, v52, v29, v57
	v_pk_fma_f16 v11, v47, v27, v55
	s_waitcnt vmcnt(10)
	v_pk_fma_f16 v20, v51, v36, v56
	v_pk_fma_f16 v18, v46, v34, v53
	v_pk_fma_f16 v21, v52, v37, v57
	v_pk_fma_f16 v19, v47, v35, v55
	ds_write_b128 v42, v[10:13] offset:4352
	ds_write_b128 v42, v[18:21] offset:21760
	v_pk_add_f16 v36, v13, v21
	v_pk_add_f16 v38, v12, v20
	v_pk_add_f16 v41, v11, v19
	v_pk_add_f16 v43, v10, v18
	v_pk_fma_f16 v12, v51, v32, v56
	v_pk_fma_f16 v10, v46, v30, v53
	v_pk_fma_f16 v13, v52, v33, v57
	v_pk_fma_f16 v11, v47, v31, v55
	s_waitcnt vmcnt(9)
	v_pk_fma_f16 v20, v51, v64, v56
	v_pk_fma_f16 v18, v46, v62, v53
	v_pk_fma_f16 v21, v52, v65, v57
	v_pk_fma_f16 v19, v47, v63, v55
	ds_write_b128 v42, v[10:13] offset:8704
	ds_write_b128 v42, v[18:21] offset:26112
	v_pk_add_f16 v30, v13, v21
	v_pk_add_f16 v31, v12, v20
	v_pk_add_f16 v33, v11, v19
	v_pk_add_f16 v35, v10, v18
	v_pk_fma_f16 v12, v51, v60, v56
	v_pk_fma_f16 v10, v46, v58, v53
	v_pk_fma_f16 v13, v52, v61, v57
	v_pk_fma_f16 v11, v47, v59, v55
	s_waitcnt vmcnt(8)
	v_pk_fma_f16 v18, v46, v66, v53
	v_pk_fma_f16 v20, v51, v68, v56
	v_pk_fma_f16 v21, v52, v69, v57
	v_pk_fma_f16 v19, v47, v67, v55
	ds_write_b128 v42, v[10:13] offset:13056
	ds_write_b128 v42, v[18:21] offset:30464
	s_waitcnt lgkmcnt(0)
	s_barrier
	v_pk_add_f16 v29, v10, v18
	v_add_u32_e32 v10, s20, v39
	v_lshl_or_b32 v18, v10, 8, v40
	v_pk_add_f16 v28, v11, v19
	v_add_u32_e32 v10, 0x1000, v18
	v_add_u32_e32 v19, 0x2000, v18
	v_pk_add_f16 v26, v13, v21
	v_pk_add_f16 v27, v12, v20
	buffer_load_dwordx4 v[60:63], v18, s[8:11], 0 offen sc1
	buffer_load_dwordx4 v[64:67], v10, s[8:11], 0 offen sc1
	v_add_u32_e32 v20, 0x3000, v18
	buffer_load_dwordx4 v[86:89], v19, s[8:11], 0 offen sc1
	buffer_load_dwordx4 v[10:13], v20, s[8:11], 0 offen sc1
	v_add_u32_e32 v19, 0x4000, v18
	v_add_u32_e32 v20, 0x5000, v18
	buffer_load_dwordx4 v[90:93], v19, s[8:11], 0 offen sc1
	buffer_load_dwordx4 v[94:97], v20, s[8:11], 0 offen sc1
	v_add_u32_e32 v32, 0x6000, v18
	v_add_u32_e32 v34, 0x7000, v18
	buffer_load_dwordx4 v[98:101], v32, s[8:11], 0 offen sc1
	buffer_load_dwordx4 v[18:21], v34, s[8:11], 0 offen sc1
	v_mov_b32_e32 v32, v0
	s_waitcnt vmcnt(15)
	v_pk_fma_f16 v72, v51, v72, v56
	v_add_u32_e32 v34, 0xffffff00, v32
	v_lshlrev_b32_e32 v32, 4, v32
	v_ashrrev_i32_e32 v59, 4, v34
	v_and_b32_e32 v102, 0xf0, v32
	v_pk_fma_f16 v70, v46, v70, v53
	v_pk_fma_f16 v73, v52, v73, v57
	v_pk_fma_f16 v71, v47, v71, v55
	s_waitcnt vmcnt(11)
	v_pk_fma_f16 v78, v46, v78, v53
	v_pk_fma_f16 v79, v47, v79, v55
	v_mad_u64_u32 v[104:105], s[22:23], v59, s13, v[102:103]
	v_pk_fma_f16 v80, v51, v80, v56
	v_pk_fma_f16 v81, v52, v81, v57
	ds_write_b128 v104, v[70:73] offset:34816
	ds_write_b128 v104, v[78:81] offset:52224
	v_pk_add_f16 v117, v71, v79
	v_pk_add_f16 v118, v70, v78
	v_pk_fma_f16 v70, v51, v76, v56
	v_pk_fma_f16 v68, v46, v74, v53
	v_pk_fma_f16 v71, v52, v77, v57
	v_pk_fma_f16 v69, v47, v75, v55
	v_pk_fma_f16 v16, v51, v16, v56
	v_pk_fma_f16 v14, v46, v14, v53
	v_pk_fma_f16 v17, v52, v17, v57
	v_pk_fma_f16 v15, v47, v15, v55
	v_pk_fma_f16 v4, v51, v4, v56
	v_pk_fma_f16 v2, v46, v2, v53
	v_pk_fma_f16 v5, v52, v5, v57
	v_pk_fma_f16 v3, v47, v3, v55
	s_waitcnt vmcnt(8)
	v_pk_fma_f16 v6, v46, v6, v53
	v_pk_add_f16 v115, v73, v81
	v_pk_add_f16 v116, v72, v80
	v_pk_fma_f16 v74, v51, v84, v56
	v_pk_fma_f16 v72, v46, v82, v53
	v_pk_fma_f16 v75, v52, v85, v57
	v_pk_fma_f16 v73, v47, v83, v55
	ds_write_b128 v104, v[68:71] offset:39168
	ds_write_b128 v104, v[72:75] offset:56576
	v_pk_fma_f16 v24, v51, v24, v56
	v_pk_fma_f16 v22, v46, v22, v53
	v_pk_fma_f16 v25, v52, v25, v57
	v_pk_fma_f16 v23, v47, v23, v55
	ds_write_b128 v104, v[14:17] offset:43520
	ds_write_b128 v104, v[22:25] offset:60928
	v_pk_fma_f16 v8, v51, v8, v56
	v_pk_fma_f16 v9, v52, v9, v57
	v_pk_fma_f16 v7, v47, v7, v55
	ds_write_b128 v104, v[2:5] offset:47872
	ds_write_b128 v104, v[6:9] offset:65280
	v_pk_add_f16 v39, v2, v6
	v_add_u32_e32 v2, s18, v59
	v_lshl_or_b32 v6, v2, 8, v102
	v_pk_add_f16 v34, v4, v8
	v_pk_add_f16 v37, v3, v7
	v_add_u32_e32 v2, 0x1000, v6
	v_add_u32_e32 v7, 0x2000, v6
	v_add_u32_e32 v8, 0x3000, v6
	v_pk_add_f16 v50, v71, v75
	v_pk_add_f16 v58, v70, v74
	v_pk_add_f16 v119, v69, v73
	v_pk_add_f16 v120, v68, v72
	v_pk_add_f16 v40, v17, v25
	v_pk_add_f16 v42, v16, v24
	v_pk_add_f16 v45, v15, v23
	v_pk_add_f16 v49, v14, v22
	v_pk_add_f16 v32, v5, v9
	buffer_load_dwordx4 v[68:71], v6, s[8:11], 0 offen sc1
	buffer_load_dwordx4 v[72:75], v2, s[8:11], 0 offen sc1
	buffer_load_dwordx4 v[14:17], v7, s[8:11], 0 offen sc1
	s_nop 0
	buffer_load_dwordx4 v[2:5], v8, s[8:11], 0 offen sc1
	v_add_u32_e32 v7, 0x4000, v6
	v_add_u32_e32 v8, 0x5000, v6
	v_add_u32_e32 v59, 0x6000, v6
	buffer_load_dwordx4 v[76:79], v7, s[8:11], 0 offen sc1
	buffer_load_dwordx4 v[80:83], v8, s[8:11], 0 offen sc1
	v_add_u32_e32 v84, 0x7000, v6
	buffer_load_dwordx4 v[22:25], v59, s[8:11], 0 offen sc1
	buffer_load_dwordx4 v[6:9], v84, s[8:11], 0 offen sc1
	v_mov_b32_e32 v59, v0
	v_fma_mix_f32 v192, v114, s44, 0 op_sel_hi:[1,0,0]
	v_fma_mix_f32 v193, v114, s44, 0 op_sel:[1,0,0] op_sel_hi:[1,0,0]
	v_fma_mix_f32 v192, v118, s44, v192 op_sel_hi:[1,0,0]
	v_fma_mix_f32 v193, v118, s44, v193 op_sel:[1,0,0] op_sel_hi:[1,0,0]
	v_fma_mix_f32 v194, v54, s44, 0 op_sel_hi:[1,0,0]
	v_fma_mix_f32 v195, v54, s44, 0 op_sel:[1,0,0] op_sel_hi:[1,0,0]
	v_fma_mix_f32 v194, v117, s44, v194 op_sel_hi:[1,0,0]
	v_fma_mix_f32 v195, v117, s44, v195 op_sel:[1,0,0] op_sel_hi:[1,0,0]
	v_fma_mix_f32 v196, v48, s44, 0 op_sel_hi:[1,0,0]
	v_fma_mix_f32 v197, v48, s44, 0 op_sel:[1,0,0] op_sel_hi:[1,0,0]
	v_fma_mix_f32 v196, v116, s44, v196 op_sel_hi:[1,0,0]
	v_fma_mix_f32 v197, v116, s44, v197 op_sel:[1,0,0] op_sel_hi:[1,0,0]
	v_fma_mix_f32 v198, v44, s44, 0 op_sel_hi:[1,0,0]
	v_fma_mix_f32 v199, v44, s44, 0 op_sel:[1,0,0] op_sel_hi:[1,0,0]
	v_fma_mix_f32 v198, v115, s44, v198 op_sel_hi:[1,0,0]
	v_fma_mix_f32 v199, v115, s44, v199 op_sel:[1,0,0] op_sel_hi:[1,0,0]
	v_fma_mix_f32 v200, v43, s44, 0 op_sel_hi:[1,0,0]
	v_fma_mix_f32 v201, v43, s44, 0 op_sel:[1,0,0] op_sel_hi:[1,0,0]
	v_fma_mix_f32 v200, v120, s44, v200 op_sel_hi:[1,0,0]
	v_fma_mix_f32 v201, v120, s44, v201 op_sel:[1,0,0] op_sel_hi:[1,0,0]
	v_fma_mix_f32 v202, v41, s44, 0 op_sel_hi:[1,0,0]
	v_fma_mix_f32 v203, v41, s44, 0 op_sel:[1,0,0] op_sel_hi:[1,0,0]
	v_fma_mix_f32 v202, v119, s44, v202 op_sel_hi:[1,0,0]
	v_fma_mix_f32 v203, v119, s44, v203 op_sel:[1,0,0] op_sel_hi:[1,0,0]
	v_fma_mix_f32 v204, v38, s44, 0 op_sel_hi:[1,0,0]
	v_fma_mix_f32 v205, v38, s44, 0 op_sel:[1,0,0] op_sel_hi:[1,0,0]
	v_fma_mix_f32 v204, v58, s44, v204 op_sel_hi:[1,0,0]
	v_fma_mix_f32 v205, v58, s44, v205 op_sel:[1,0,0] op_sel_hi:[1,0,0]
	v_fma_mix_f32 v206, v36, s44, 0 op_sel_hi:[1,0,0]
	v_fma_mix_f32 v207, v36, s44, 0 op_sel:[1,0,0] op_sel_hi:[1,0,0]
	v_fma_mix_f32 v206, v50, s44, v206 op_sel_hi:[1,0,0]
	v_fma_mix_f32 v207, v50, s44, v207 op_sel:[1,0,0] op_sel_hi:[1,0,0]
	v_fma_mix_f32 v208, v35, s44, 0 op_sel_hi:[1,0,0]
	v_fma_mix_f32 v209, v35, s44, 0 op_sel:[1,0,0] op_sel_hi:[1,0,0]
	v_fma_mix_f32 v208, v49, s44, v208 op_sel_hi:[1,0,0]
	v_fma_mix_f32 v209, v49, s44, v209 op_sel:[1,0,0] op_sel_hi:[1,0,0]
	v_fma_mix_f32 v210, v33, s44, 0 op_sel_hi:[1,0,0]
	v_fma_mix_f32 v211, v33, s44, 0 op_sel:[1,0,0] op_sel_hi:[1,0,0]
	v_fma_mix_f32 v210, v45, s44, v210 op_sel_hi:[1,0,0]
	v_fma_mix_f32 v211, v45, s44, v211 op_sel:[1,0,0] op_sel_hi:[1,0,0]
	v_fma_mix_f32 v212, v31, s44, 0 op_sel_hi:[1,0,0]
	v_fma_mix_f32 v213, v31, s44, 0 op_sel:[1,0,0] op_sel_hi:[1,0,0]
	v_fma_mix_f32 v212, v42, s44, v212 op_sel_hi:[1,0,0]
	v_fma_mix_f32 v213, v42, s44, v213 op_sel:[1,0,0] op_sel_hi:[1,0,0]
	v_fma_mix_f32 v214, v30, s44, 0 op_sel_hi:[1,0,0]
	v_fma_mix_f32 v215, v30, s44, 0 op_sel:[1,0,0] op_sel_hi:[1,0,0]
	v_fma_mix_f32 v214, v40, s44, v214 op_sel_hi:[1,0,0]
	v_fma_mix_f32 v215, v40, s44, v215 op_sel:[1,0,0] op_sel_hi:[1,0,0]
	v_fma_mix_f32 v216, v29, s44, 0 op_sel_hi:[1,0,0]
	v_fma_mix_f32 v217, v29, s44, 0 op_sel:[1,0,0] op_sel_hi:[1,0,0]
	v_fma_mix_f32 v216, v39, s44, v216 op_sel_hi:[1,0,0]
	v_fma_mix_f32 v217, v39, s44, v217 op_sel:[1,0,0] op_sel_hi:[1,0,0]
	v_fma_mix_f32 v218, v28, s44, 0 op_sel_hi:[1,0,0]
	v_fma_mix_f32 v219, v28, s44, 0 op_sel:[1,0,0] op_sel_hi:[1,0,0]
	v_fma_mix_f32 v218, v37, s44, v218 op_sel_hi:[1,0,0]
	v_fma_mix_f32 v219, v37, s44, v219 op_sel:[1,0,0] op_sel_hi:[1,0,0]
	v_fma_mix_f32 v220, v27, s44, 0 op_sel_hi:[1,0,0]
	v_fma_mix_f32 v221, v27, s44, 0 op_sel:[1,0,0] op_sel_hi:[1,0,0]
	v_fma_mix_f32 v220, v34, s44, v220 op_sel_hi:[1,0,0]
	v_fma_mix_f32 v221, v34, s44, v221 op_sel:[1,0,0] op_sel_hi:[1,0,0]
	v_fma_mix_f32 v222, v26, s44, 0 op_sel_hi:[1,0,0]
	v_fma_mix_f32 v223, v26, s44, 0 op_sel:[1,0,0] op_sel_hi:[1,0,0]
	v_fma_mix_f32 v222, v32, s44, v222 op_sel_hi:[1,0,0]
	v_fma_mix_f32 v223, v32, s44, v223 op_sel:[1,0,0] op_sel_hi:[1,0,0]
	s_waitcnt lgkmcnt(0)
	s_barrier
	s_lshl_b32 s8, s12, 16
	v_add_u32_e32 v85, 0xffffff00, v59
	v_lshlrev_b32_e32 v84, 3, v59
	v_lshrrev_b32_e32 v121, 4, v85
	v_and_b32_e32 v102, 56, v84
	v_lshrrev_b32_e32 v110, 3, v85
	v_ashrrev_i32_e32 v85, 3, v85
	s_movk_i32 s10, 0xffc0
	s_or_b32 s8, s8, s17
	v_lshl_or_b32 v84, v102, 1, v122
	v_bfi_b32 v85, s10, v85, v110
	s_movk_i32 s11, 0x90
	v_or_b32_e32 v106, s8, v102
	v_mad_u64_u32 v[102:103], s[8:9], v85, s11, v[84:85]
	ds_read_b128 v[102:105], v102
	v_lshlrev_b32_e32 v123, 1, v106
	v_lshrrev_b32_e32 v111, 3, v59
	v_ashrrev_i32_e32 v106, 3, v59
	v_lshl_add_u32 v85, v85, 8, v123
	v_bfi_b32 v112, s10, v106, v111
	v_mad_u64_u32 v[106:107], s[8:9], v112, s11, v[84:85]
	ds_read_b128 v[106:109], v106
	s_waitcnt lgkmcnt(1)
	buffer_store_dwordx4 v[102:105], v85, s[4:7], 0 offen sc1
	v_add_u32_e32 v85, 0x100, v59
	v_ashrrev_i32_e32 v85, 3, v85
	v_bfi_b32 v125, s10, v85, v110
	v_mad_u64_u32 v[102:103], s[8:9], v125, s11, v[84:85]
	v_add_u32_e32 v85, 0x200, v59
	v_ashrrev_i32_e32 v85, 3, v85
	v_bfi_b32 v126, s10, v85, v111
	ds_read_b128 v[102:105], v102
	v_mad_u64_u32 v[84:85], s[8:9], v126, s11, v[84:85]
	v_lshl_add_u32 v124, v112, 8, v123
	ds_read_b128 v[110:113], v84
	v_lshl_add_u32 v84, v125, 8, v123
	s_waitcnt lgkmcnt(2)
	buffer_store_dwordx4 v[106:109], v124, s[4:7], 0 offen sc1
	s_waitcnt lgkmcnt(1)
	buffer_store_dwordx4 v[102:105], v84, s[4:7], 0 offen sc1
	v_lshl_add_u32 v84, v126, 8, v123
	v_lshlrev_b32_e32 v59, 4, v59
	s_waitcnt lgkmcnt(0)
	buffer_store_dwordx4 v[110:113], v84, s[4:7], 0 offen sc1
	v_and_b32_e32 v84, 0xf0, v59
	s_waitcnt vmcnt(19)
	v_pk_fma_f16 v63, v52, v63, v57
	v_pk_fma_f16 v62, v51, v62, v56
	v_pk_fma_f16 v61, v47, v61, v55
	v_pk_fma_f16 v60, v46, v60, v53
	s_waitcnt vmcnt(15)
	v_pk_fma_f16 v93, v52, v93, v57
	v_pk_fma_f16 v92, v51, v92, v56
	v_pk_fma_f16 v91, v47, v91, v55
	v_pk_fma_f16 v90, v46, v90, v53
	v_mad_u64_u32 v[84:85], s[8:9], v121, s13, v[84:85]
	ds_write_b128 v84, v[60:63]
	ds_write_b128 v84, v[90:93] offset:17408
	v_pk_add_f16 v59, v63, v93
	v_pk_add_f16 v85, v62, v92
	v_pk_add_f16 v91, v61, v91
	v_pk_add_f16 v90, v60, v90
	v_pk_fma_f16 v63, v52, v67, v57
	v_pk_fma_f16 v62, v51, v66, v56
	v_pk_fma_f16 v61, v47, v65, v55
	v_pk_fma_f16 v60, v46, v64, v53
	s_waitcnt vmcnt(14)
	v_pk_fma_f16 v67, v52, v97, v57
	v_pk_fma_f16 v66, v51, v96, v56
	v_pk_fma_f16 v65, v47, v95, v55
	v_pk_fma_f16 v64, v46, v94, v53
	ds_write_b128 v84, v[60:63] offset:4352
	ds_write_b128 v84, v[64:67] offset:21760
	v_pk_add_f16 v92, v63, v67
	v_pk_add_f16 v93, v62, v66
	v_pk_add_f16 v94, v61, v65
	v_pk_add_f16 v95, v60, v64
	v_pk_fma_f16 v63, v52, v89, v57
	v_pk_fma_f16 v62, v51, v88, v56
	v_pk_fma_f16 v61, v47, v87, v55
	v_pk_fma_f16 v60, v46, v86, v53
	s_waitcnt vmcnt(13)
	v_pk_fma_f16 v67, v52, v101, v57
	v_pk_fma_f16 v66, v51, v100, v56
	v_pk_fma_f16 v65, v47, v99, v55
	v_pk_fma_f16 v64, v46, v98, v53
	ds_write_b128 v84, v[60:63] offset:8704
	ds_write_b128 v84, v[64:67] offset:26112
	v_pk_add_f16 v86, v63, v67
	v_pk_add_f16 v87, v62, v66
	v_pk_add_f16 v88, v61, v65
	v_pk_add_f16 v89, v60, v64
	v_pk_fma_f16 v63, v52, v13, v57
	v_pk_fma_f16 v62, v51, v12, v56
	v_pk_fma_f16 v61, v47, v11, v55
	v_pk_fma_f16 v60, v46, v10, v53
	v_mov_b32_e32 v97, v0
	s_waitcnt vmcnt(12)
	v_pk_fma_f16 v21, v52, v21, v57
	v_pk_fma_f16 v20, v51, v20, v56
	v_pk_fma_f16 v19, v47, v19, v55
	v_pk_fma_f16 v18, v46, v18, v53
	ds_write_b128 v84, v[60:63] offset:13056
	ds_write_b128 v84, v[18:21] offset:30464
	s_waitcnt lgkmcnt(0)
	s_barrier
	v_pk_add_f16 v96, v60, v18
	v_add_u32_e32 v13, 0xffffff00, v97
	v_lshlrev_b32_e32 v12, 3, v97
	v_lshrrev_b32_e32 v98, 4, v13
	v_and_b32_e32 v18, 56, v12
	v_lshrrev_b32_e32 v64, 3, v13
	v_ashrrev_i32_e32 v13, 3, v13
	v_lshl_or_b32 v12, v18, 1, v122
	v_bfi_b32 v13, s10, v13, v64
	v_pk_add_f16 v84, v61, v19
	v_or_b32_e32 v60, s2, v18
	v_mad_u64_u32 v[18:19], s[8:9], v13, s11, v[12:13]
	v_pk_add_f16 v10, v63, v21
	v_pk_add_f16 v11, v62, v20
	ds_read_b128 v[18:21], v18 offset:18432
	v_lshlrev_b32_e32 v99, 1, v60
	v_lshrrev_b32_e32 v65, 3, v97
	v_ashrrev_i32_e32 v60, 3, v97
	v_lshl_add_u32 v13, v13, 8, v99
	v_bfi_b32 v66, s10, v60, v65
	v_mad_u64_u32 v[60:61], s[8:9], v66, s11, v[12:13]
	ds_read_b128 v[60:63], v60 offset:18432
	s_waitcnt lgkmcnt(1)
	buffer_store_dwordx4 v[18:21], v13, s[4:7], 0 offen sc1
	v_add_u32_e32 v13, 0x100, v97
	v_ashrrev_i32_e32 v13, 3, v13
	v_bfi_b32 v101, s10, v13, v64
	v_mad_u64_u32 v[18:19], s[8:9], v101, s11, v[12:13]
	v_add_u32_e32 v13, 0x200, v97
	v_ashrrev_i32_e32 v13, 3, v13
	v_bfi_b32 v102, s10, v13, v65
	ds_read_b128 v[18:21], v18 offset:18432
	v_mad_u64_u32 v[12:13], s[8:9], v102, s11, v[12:13]
	v_lshl_add_u32 v100, v66, 8, v99
	ds_read_b128 v[64:67], v12 offset:18432
	v_lshl_add_u32 v12, v101, 8, v99
	s_waitcnt lgkmcnt(2)
	buffer_store_dwordx4 v[60:63], v100, s[4:7], 0 offen sc1
	s_waitcnt lgkmcnt(1)
	buffer_store_dwordx4 v[18:21], v12, s[4:7], 0 offen sc1
	v_lshl_add_u32 v12, v102, 8, v99
	s_waitcnt lgkmcnt(0)
	buffer_store_dwordx4 v[64:67], v12, s[4:7], 0 offen sc1
	v_lshlrev_b32_e32 v12, 4, v97
	v_and_b32_e32 v12, 0xf0, v12
	s_waitcnt vmcnt(15)
	v_pk_fma_f16 v21, v52, v71, v57
	v_pk_fma_f16 v20, v51, v70, v56
	v_pk_fma_f16 v19, v47, v69, v55
	v_pk_fma_f16 v18, v46, v68, v53
	s_waitcnt vmcnt(11)
	v_pk_fma_f16 v63, v52, v79, v57
	v_pk_fma_f16 v62, v51, v78, v56
	v_pk_fma_f16 v61, v47, v77, v55
	v_pk_fma_f16 v60, v46, v76, v53
	v_mad_u64_u32 v[12:13], s[8:9], v98, s13, v[12:13]
	ds_write_b128 v12, v[18:21] offset:34816
	ds_write_b128 v12, v[60:63] offset:52224
	v_pk_add_f16 v13, v21, v63
	v_pk_add_f16 v64, v20, v62
	v_pk_add_f16 v65, v19, v61
	v_pk_add_f16 v66, v18, v60
	v_pk_fma_f16 v21, v52, v75, v57
	v_pk_fma_f16 v20, v51, v74, v56
	v_pk_fma_f16 v19, v47, v73, v55
	v_pk_fma_f16 v18, v46, v72, v53
	s_waitcnt vmcnt(10)
	v_pk_fma_f16 v63, v52, v83, v57
	v_pk_fma_f16 v62, v51, v82, v56
	v_pk_fma_f16 v61, v47, v81, v55
	v_pk_fma_f16 v60, v46, v80, v53
	v_pk_fma_f16 v17, v52, v17, v57
	v_pk_fma_f16 v16, v51, v16, v56
	v_pk_fma_f16 v15, v47, v15, v55
	v_pk_fma_f16 v14, v46, v14, v53
	v_pk_fma_f16 v5, v52, v5, v57
	v_pk_fma_f16 v4, v51, v4, v56
	v_pk_fma_f16 v3, v47, v3, v55
	v_pk_fma_f16 v2, v46, v2, v53
	s_waitcnt vmcnt(8)
	v_pk_fma_f16 v7, v47, v7, v55
	v_pk_fma_f16 v6, v46, v6, v53
	ds_write_b128 v12, v[18:21] offset:39168
	ds_write_b128 v12, v[60:63] offset:56576
	v_pk_add_f16 v63, v21, v63
	v_pk_add_f16 v62, v20, v62
	v_pk_add_f16 v61, v19, v61
	v_pk_add_f16 v60, v18, v60
	v_pk_fma_f16 v21, v52, v25, v57
	v_pk_fma_f16 v20, v51, v24, v56
	v_pk_fma_f16 v19, v47, v23, v55
	v_pk_fma_f16 v18, v46, v22, v53
	ds_write_b128 v12, v[14:17] offset:43520
	ds_write_b128 v12, v[18:21] offset:60928
	v_pk_fma_f16 v9, v52, v9, v57
	v_pk_fma_f16 v8, v51, v8, v56
	ds_write_b128 v12, v[2:5] offset:47872
	ds_write_b128 v12, v[6:9] offset:65280
	v_pk_add_f16 v24, v3, v7
	v_pk_add_f16 v25, v2, v6
	v_pk_add_f16 v22, v5, v9
	v_pk_add_f16 v23, v4, v8
	v_fma_mix_f32 v192, v90, s44, v192 op_sel_hi:[1,0,0]
	v_fma_mix_f32 v193, v90, s44, v193 op_sel:[1,0,0] op_sel_hi:[1,0,0]
	v_fma_mixlo_f16 v224, v66, s44, v192 op_sel_hi:[1,0,0]
	v_pk_add_f16 v19, v15, v19
	v_fma_mixhi_f16 v224, v66, s44, v193 op_sel:[1,0,0] op_sel_hi:[1,0,0]
	v_fma_mix_f32 v194, v91, s44, v194 op_sel_hi:[1,0,0]
	v_fma_mix_f32 v195, v91, s44, v195 op_sel:[1,0,0] op_sel_hi:[1,0,0]
	v_pk_add_f16 v18, v14, v18
	v_fma_mixlo_f16 v225, v65, s44, v194 op_sel_hi:[1,0,0]
	s_nop 0
	v_fma_mixhi_f16 v225, v65, s44, v195 op_sel:[1,0,0] op_sel_hi:[1,0,0]
	s_mov_b32 s2, 0x3e000000
	v_fma_mix_f32 v196, v85, s44, v196 op_sel_hi:[1,0,0]
	v_fma_mix_f32 v197, v85, s44, v197 op_sel:[1,0,0] op_sel_hi:[1,0,0]
	v_fma_mixlo_f16 v226, v64, s44, v196 op_sel_hi:[1,0,0]
	v_pk_add_f16 v21, v17, v21
	v_fma_mixhi_f16 v226, v64, s44, v197 op_sel:[1,0,0] op_sel_hi:[1,0,0]
	v_fma_mix_f32 v198, v59, s44, v198 op_sel_hi:[1,0,0]
	v_fma_mix_f32 v199, v59, s44, v199 op_sel:[1,0,0] op_sel_hi:[1,0,0]
	v_pk_add_f16 v20, v16, v20
	v_fma_mixlo_f16 v227, v13, s44, v198 op_sel_hi:[1,0,0]
	v_fma_mix_f32 v200, v60, s44, v200 op_sel_hi:[1,0,0]
	v_fma_mixhi_f16 v227, v13, s44, v199 op_sel:[1,0,0] op_sel_hi:[1,0,0]
	v_add_u32_e32 v16, 0x1a000, v12
	v_fma_mix_f32 v201, v60, s44, v201 op_sel:[1,0,0] op_sel_hi:[1,0,0]
	ds_write_b128 v16, v[224:227]
	v_fma_mixlo_f16 v228, v95, s44, v200 op_sel_hi:[1,0,0]
	v_fma_mix_f32 v202, v61, s44, v202 op_sel_hi:[1,0,0]
	v_fma_mixhi_f16 v228, v95, s44, v201 op_sel:[1,0,0] op_sel_hi:[1,0,0]
	s_nop 0
	v_fma_mixlo_f16 v229, v94, s44, v202 op_sel_hi:[1,0,0]
	v_fma_mix_f32 v203, v94, s44, v203 op_sel:[1,0,0] op_sel_hi:[1,0,0]
	v_fma_mixhi_f16 v229, v61, s44, v203 op_sel:[1,0,0] op_sel_hi:[1,0,0]
	v_fma_mix_f32 v204, v93, s44, v204 op_sel_hi:[1,0,0]
	v_fma_mix_f32 v205, v93, s44, v205 op_sel:[1,0,0] op_sel_hi:[1,0,0]
	v_fma_mixlo_f16 v230, v62, s44, v204 op_sel_hi:[1,0,0]
	v_fma_mix_f32 v206, v63, s44, v206 op_sel_hi:[1,0,0]
	v_fma_mixhi_f16 v230, v62, s44, v205 op_sel:[1,0,0] op_sel_hi:[1,0,0]
	s_nop 0
	v_fma_mixlo_f16 v231, v92, s44, v206 op_sel_hi:[1,0,0]
	v_fma_mix_f32 v207, v92, s44, v207 op_sel:[1,0,0] op_sel_hi:[1,0,0]
	v_fma_mixhi_f16 v231, v63, s44, v207 op_sel:[1,0,0] op_sel_hi:[1,0,0]
	v_fma_mix_f32 v208, v18, s44, v208 op_sel_hi:[1,0,0]
	v_fma_mix_f32 v209, v18, s44, v209 op_sel:[1,0,0] op_sel_hi:[1,0,0]
	v_fma_mix_f32 v210, v19, s44, v210 op_sel_hi:[1,0,0]
	ds_write_b128 v16, v[228:231] offset:4352
	v_fma_mixlo_f16 v232, v89, s44, v208 op_sel_hi:[1,0,0]
	s_nop 0
	v_fma_mixhi_f16 v232, v89, s44, v209 op_sel:[1,0,0] op_sel_hi:[1,0,0]
	v_fma_mix_f32 v211, v19, s44, v211 op_sel:[1,0,0] op_sel_hi:[1,0,0]
	v_fma_mixlo_f16 v233, v88, s44, v210 op_sel_hi:[1,0,0]
	s_nop 0
	v_fma_mixhi_f16 v233, v88, s44, v211 op_sel:[1,0,0] op_sel_hi:[1,0,0]
	v_fma_mix_f32 v212, v87, s44, v212 op_sel_hi:[1,0,0]
	v_fma_mix_f32 v213, v87, s44, v213 op_sel:[1,0,0] op_sel_hi:[1,0,0]
	v_fma_mixlo_f16 v234, v20, s44, v212 op_sel_hi:[1,0,0]
	v_fma_mix_f32 v214, v21, s44, v214 op_sel_hi:[1,0,0]
	v_fma_mixhi_f16 v234, v20, s44, v213 op_sel:[1,0,0] op_sel_hi:[1,0,0]
	s_nop 0
	v_fma_mixlo_f16 v235, v86, s44, v214 op_sel_hi:[1,0,0]
	v_fma_mix_f32 v215, v86, s44, v215 op_sel:[1,0,0] op_sel_hi:[1,0,0]
	v_fma_mixhi_f16 v235, v21, s44, v215 op_sel:[1,0,0] op_sel_hi:[1,0,0]
	v_fma_mix_f32 v216, v25, s44, v216 op_sel_hi:[1,0,0]
	v_fma_mix_f32 v217, v25, s44, v217 op_sel:[1,0,0] op_sel_hi:[1,0,0]
	v_fma_mix_f32 v218, v24, s44, v218 op_sel_hi:[1,0,0]
	ds_write_b128 v16, v[232:235] offset:8704
	v_fma_mixlo_f16 v236, v96, s44, v216 op_sel_hi:[1,0,0]
	s_nop 0
	v_fma_mixhi_f16 v236, v96, s44, v217 op_sel:[1,0,0] op_sel_hi:[1,0,0]
	v_fma_mix_f32 v219, v24, s44, v219 op_sel:[1,0,0] op_sel_hi:[1,0,0]
	v_fma_mixlo_f16 v237, v84, s44, v218 op_sel_hi:[1,0,0]
	s_nop 0
	v_fma_mixhi_f16 v237, v84, s44, v219 op_sel:[1,0,0] op_sel_hi:[1,0,0]
	v_fma_mix_f32 v220, v11, s44, v220 op_sel_hi:[1,0,0]
	v_fma_mix_f32 v221, v11, s44, v221 op_sel:[1,0,0] op_sel_hi:[1,0,0]
	v_fma_mixlo_f16 v238, v23, s44, v220 op_sel_hi:[1,0,0]
	s_nop 0
	v_fma_mixhi_f16 v238, v23, s44, v221 op_sel:[1,0,0] op_sel_hi:[1,0,0]
	v_fma_mix_f32 v223, v22, s44, v223 op_sel:[1,0,0] op_sel_hi:[1,0,0]
	v_fma_mix_f32 v222, v10, s44, v222 op_sel_hi:[1,0,0]
	v_fma_mixhi_f16 v239, v10, s44, v223 op_sel:[1,0,0] op_sel_hi:[1,0,0]
	s_nop 0
	v_fma_mixlo_f16 v239, v22, s44, v222 op_sel_hi:[1,0,0]
	s_cmpk_lt_u32 s15, 0x180
	s_cselect_b64 s[8:9], -1, 0
	s_cmpk_gt_u32 s15, 0x17f
	ds_write_b128 v16, v[236:239] offset:13056
	s_cbranch_scc1 .LBB2_3
	s_load_dwordx2 s[10:11], s[0:1], 0x78
	s_load_dwordx4 s[24:27], s[0:1], 0x50
	v_mov_b32_e32 v2, v0
	s_ashr_i32 s13, s12, 31
	s_lshl_b64 s[22:23], s[12:13], 12
	s_waitcnt lgkmcnt(0)
	s_add_u32 s10, s10, s22
	v_lshlrev_b32_e32 v2, 3, v2
	s_addc_u32 s11, s11, s23
	v_and_b32_e32 v2, 0x1f8, v2
	global_load_dwordx2 v[136:137], v2, s[10:11]
	global_load_dwordx2 v[132:133], v2, s[10:11] offset:512
	global_load_dwordx2 v[128:129], v2, s[10:11] offset:1024
	global_load_dwordx2 v[124:125], v2, s[10:11] offset:1536
	global_load_dwordx2 v[134:135], v2, s[10:11] offset:2048
	global_load_dwordx2 v[130:131], v2, s[10:11] offset:2560
	global_load_dwordx2 v[126:127], v2, s[10:11] offset:3072
	global_load_dwordx2 v[122:123], v2, s[10:11] offset:3584
	s_lshl_b32 s2, s14, 4
	s_lshl_b32 s10, s19, 3
	s_add_i32 s10, s10, s2
	s_sub_i32 s2, s10, 32
	s_lshl_b64 s[2:3], s[2:3], 10
	v_lshl_or_b32 v2, v2, 1, s2
	v_mov_b32_e32 v3, s3
	v_lshl_add_u64 v[4:5], s[24:25], 0, v[2:3]
	global_load_dwordx4 v[18:21], v[4:5], off
	global_load_dwordx4 v[102:105], v[4:5], off offset:1024
	global_load_dwordx4 v[94:97], v[4:5], off offset:2048
	global_load_dwordx4 v[86:89], v[4:5], off offset:3072
	v_add_co_u32_e32 v4, vcc, s21, v4
	v_lshl_add_u64 v[6:7], s[26:27], 0, v[2:3]
	s_nop 0
	v_addc_co_u32_e32 v5, vcc, 0, v5, vcc
	global_load_dwordx4 v[78:81], v[4:5], off
	global_load_dwordx4 v[74:77], v[4:5], off offset:1024
	global_load_dwordx4 v[70:73], v[4:5], off offset:2048
	global_load_dwordx4 v[66:69], v[4:5], off offset:3072
	s_nop 0
	global_load_dwordx4 v[2:5], v[6:7], off
	global_load_dwordx4 v[118:121], v[6:7], off offset:1024
	global_load_dwordx4 v[114:117], v[6:7], off offset:2048
	global_load_dwordx4 v[110:113], v[6:7], off offset:3072
	v_add_co_u32_e32 v6, vcc, s21, v6
	s_nop 1
	v_addc_co_u32_e32 v7, vcc, 0, v7, vcc
	global_load_dwordx4 v[106:109], v[6:7], off
	global_load_dwordx4 v[98:101], v[6:7], off offset:1024
	global_load_dwordx4 v[90:93], v[6:7], off offset:2048
	global_load_dwordx4 v[82:85], v[6:7], off offset:3072
	s_branch .LBB2_4

_Z7k_layerILi0EEvPKDF16_S1_PKfS3_S3_S3_S3_S3_S1_S1_S1_S1_S3_S3_PKhS5_PDF16_S6_PfS7_:
	s_ashr_i32 s3, s2, 1
	s_and_b32 s3, s3, -8
	s_and_b32 s16, s2, 7
	v_readfirstlane_b32 s15, v0
	s_or_b32 s12, s3, s16
	s_bfe_u32 s14, s2, 0x10003
	s_cmpk_gt_u32 s15, 0xff
	s_mov_b64 s[2:3], -1
	s_cbranch_scc0 .LBB3_17
	s_mov_b32 s44, 0x3e000000
	v_mov_b32_e32 v240, 0x64646464
	s_mov_b32 s42, 0x4010400
	s_mov_b32 s43, 0x4030402
	s_load_dwordx4 s[8:11], s[0:1], 0x0
	s_load_dwordx2 s[4:5], s[0:1], 0x80
	v_add_u32_e32 v1, 0xffffff00, v0
	s_ashr_i32 s13, s12, 31
	s_lshr_b32 s17, s15, 6
	v_ashrrev_i32_e32 v2, 4, v1
	v_lshlrev_b32_e32 v3, 3, v0
	s_lshl_b64 s[2:3], s[12:13], 14
	v_and_b32_e32 v82, 0x78, v3
	v_ashrrev_i32_e32 v3, 31, v2
	s_waitcnt lgkmcnt(0)
	s_add_u32 s2, s10, s2
	s_addc_u32 s3, s11, s3
	v_lshlrev_b64 v[4:5], 8, v[2:3]
	v_lshl_add_u64 v[4:5], s[2:3], 0, v[4:5]
	v_lshlrev_b32_e32 v6, 1, v82
	v_mov_b32_e32 v7, 0
	v_lshl_add_u64 v[4:5], v[4:5], 0, v[6:7]
	s_movk_i32 s2, 0x2000
	v_add_co_u32_e32 v8, vcc, s2, v4
	global_load_dwordx4 v[74:77], v[4:5], off
	s_nop 0
	v_addc_co_u32_e32 v9, vcc, 0, v5, vcc
	global_load_dwordx4 v[78:81], v[8:9], off offset:-4096
	global_load_dwordx4 v[66:69], v[8:9], off
	s_movk_i32 s2, 0x3000
	v_add_co_u32_e32 v4, vcc, s2, v4
	s_lshl_b32 s18, s12, 9
	s_nop 0
	v_addc_co_u32_e32 v5, vcc, 0, v5, vcc
	global_load_dwordx4 v[62:65], v[4:5], off
	v_add_u32_e32 v3, s18, v2
	s_mov_b32 s7, 0x20000
	s_mov_b32 s6, 0x1000000
	v_lshl_or_b32 v3, v3, 8, v6
	s_and_b32 s9, s9, 0xffff
	s_mov_b32 s10, s6
	s_mov_b32 s11, s7
	v_add_u32_e32 v4, 0x1000, v3
	buffer_load_dwordx4 v[58:61], v3, s[8:11], 0 offen sc1
	buffer_load_dwordx4 v[50:53], v4, s[8:11], 0 offen sc1
	v_add_u32_e32 v4, 0x2000, v3
	v_add_u32_e32 v5, 0x3000, v3
	buffer_load_dwordx4 v[42:45], v4, s[8:11], 0 offen sc1
	buffer_load_dwordx4 v[34:37], v5, s[8:11], 0 offen sc1
	v_add_u32_e32 v4, 0x4000, v3
	v_add_u32_e32 v5, 0x5000, v3
	buffer_load_dwordx4 v[70:73], v4, s[8:11], 0 offen sc1
	buffer_load_dwordx4 v[54:57], v5, s[8:11], 0 offen sc1
	v_add_u32_e32 v4, 0x6000, v3
	v_add_u32_e32 v3, 0x7000, v3
	buffer_load_dwordx4 v[46:49], v4, s[8:11], 0 offen sc1
	buffer_load_dwordx4 v[38:41], v3, s[8:11], 0 offen sc1
	s_or_b32 s2, s18, 0x80
	v_add_u32_e32 v2, s2, v2
	v_lshl_or_b32 v6, v2, 8, v6
	v_add_u32_e32 v2, 0x1000, v6
	v_add_u32_e32 v7, 0x2000, v6
	v_add_u32_e32 v8, 0x3000, v6
	buffer_load_dwordx4 v[26:29], v6, s[8:11], 0 offen sc1
	buffer_load_dwordx4 v[18:21], v2, s[8:11], 0 offen sc1
	buffer_load_dwordx4 v[10:13], v7, s[8:11], 0 offen sc1
	s_nop 0
	buffer_load_dwordx4 v[2:5], v8, s[8:11], 0 offen sc1
	v_add_u32_e32 v7, 0x4000, v6
	v_add_u32_e32 v8, 0x5000, v6
	v_add_u32_e32 v83, 0x6000, v6
	buffer_load_dwordx4 v[30:33], v7, s[8:11], 0 offen sc1
	buffer_load_dwordx4 v[22:25], v8, s[8:11], 0 offen sc1
	v_add_u32_e32 v84, 0x7000, v6
	buffer_load_dwordx4 v[14:17], v83, s[8:11], 0 offen sc1
	buffer_load_dwordx4 v[6:9], v84, s[8:11], 0 offen sc1
	v_lshlrev_b32_e32 v92, 2, v82
	v_or_b32_e32 v82, 0x1e600, v92
	s_barrier
	ds_read_b128 v[82:85], v82
	v_or_b32_e32 v86, 0x1ea00, v92
	ds_read_b128 v[88:91], v86
	v_or_b32_e32 v93, 0x1e800, v92
	v_or_b32_e32 v102, 0x1ec00, v92
	s_waitcnt lgkmcnt(1)
	v_cvt_pk_f16_f32 v82, v82, v83
	v_cvt_pk_f16_f32 v83, v84, v85
	v_or_b32_e32 v84, 0x1e610, v92
	ds_read_b128 v[84:87], v84
	v_or_b32_e32 v94, 0x1ea10, v92
	v_or_b32_e32 v108, 0x1e810, v92
	v_or_b32_e32 v109, 0x1ec10, v92
	ds_read_b128 v[94:97], v94
	ds_read_b128 v[98:101], v93
	ds_read_b128 v[102:105], v102
	s_waitcnt lgkmcnt(3)
	v_cvt_pk_f16_f32 v84, v84, v85
	s_movk_i32 s22, 0x110
	s_or_b32 s21, s18, 0x100
	s_or_b32 s19, s18, 0x180
	v_mov_b32_e32 v130, v0
	s_lshl_b32 s18, s14, 6
	v_mov_b32_e32 v132, 0x11000
	s_and_b32 s5, s5, 0xffff
	s_lshl_b32 s2, s2, 7
	s_or_b32 s2, s2, s18
	s_mov_b32 s3, 0
	s_movk_i32 s20, 0x1000
	s_waitcnt vmcnt(19)
	v_cvt_f32_f16_e32 v92, v74
	v_cvt_f32_f16_sdwa v93, v74 dst_sel:DWORD dst_unused:UNUSED_PAD src0_sel:WORD_1
	s_waitcnt vmcnt(18)
	v_cvt_f32_f16_e32 v106, v78
	v_cvt_f32_f16_sdwa v107, v78 dst_sel:DWORD dst_unused:UNUSED_PAD src0_sel:WORD_1
	v_cvt_pk_f16_f32 v74, v86, v87
	s_waitcnt lgkmcnt(1)
	v_pk_fma_f32 v[86:87], v[98:99], v[92:93], v[88:89]
	v_pk_fma_f32 v[92:93], v[98:99], v[106:107], v[88:89]
	s_waitcnt lgkmcnt(0)
	v_pk_add_f32 v[92:93], v[102:103], v[92:93]
	s_waitcnt vmcnt(17)
	v_cvt_f32_f16_e32 v106, v66
	v_cvt_f32_f16_sdwa v107, v66 dst_sel:DWORD dst_unused:UNUSED_PAD src0_sel:WORD_1
	v_cvt_pk_f16_f32 v85, v92, v93
	s_waitcnt vmcnt(16)
	v_cvt_f32_f16_e32 v92, v62
	v_cvt_f32_f16_sdwa v93, v62 dst_sel:DWORD dst_unused:UNUSED_PAD src0_sel:WORD_1
	v_cvt_f32_f16_e32 v66, v67
	v_cvt_f32_f16_sdwa v67, v67 dst_sel:DWORD dst_unused:UNUSED_PAD src0_sel:WORD_1
	v_cvt_f32_f16_e32 v62, v63
	v_cvt_f32_f16_sdwa v63, v63 dst_sel:DWORD dst_unused:UNUSED_PAD src0_sel:WORD_1
	v_pk_fma_f32 v[106:107], v[98:99], v[106:107], v[88:89]
	v_pk_fma_f32 v[88:89], v[98:99], v[92:93], v[88:89]
	v_cvt_f32_f16_e32 v92, v75
	v_cvt_f32_f16_sdwa v93, v75 dst_sel:DWORD dst_unused:UNUSED_PAD src0_sel:WORD_1
	v_cvt_f32_f16_e32 v98, v79
	v_cvt_f32_f16_sdwa v99, v79 dst_sel:DWORD dst_unused:UNUSED_PAD src0_sel:WORD_1
	v_pk_add_f32 v[88:89], v[102:103], v[88:89]
	v_pk_fma_f32 v[66:67], v[100:101], v[66:67], v[90:91]
	v_pk_fma_f32 v[62:63], v[100:101], v[62:63], v[90:91]
	v_cvt_pk_f16_f32 v75, v88, v89
	v_pk_fma_f32 v[88:89], v[100:101], v[92:93], v[90:91]
	v_pk_fma_f32 v[92:93], v[100:101], v[98:99], v[90:91]
	v_pk_add_f32 v[66:67], v[104:105], v[66:67]
	v_pk_add_f32 v[62:63], v[104:105], v[62:63]
	v_pk_add_f32 v[86:87], v[102:103], v[86:87]
	v_pk_add_f32 v[106:107], v[102:103], v[106:107]
	v_pk_add_f32 v[88:89], v[104:105], v[88:89]
	v_pk_add_f32 v[92:93], v[104:105], v[92:93]
	v_cvt_pk_f16_f32 v79, v66, v67
	ds_read_b128 v[98:101], v108
	ds_read_b128 v[102:105], v109
	v_cvt_f32_f16_e32 v66, v76
	v_cvt_f32_f16_sdwa v67, v76 dst_sel:DWORD dst_unused:UNUSED_PAD src0_sel:WORD_1
	v_cvt_pk_f16_f32 v76, v62, v63
	v_cvt_f32_f16_e32 v62, v80
	v_cvt_f32_f16_sdwa v63, v80 dst_sel:DWORD dst_unused:UNUSED_PAD src0_sel:WORD_1
	s_waitcnt lgkmcnt(1)
	v_pk_fma_f32 v[66:67], v[98:99], v[66:67], v[94:95]
	v_cvt_pk_f16_f32 v87, v86, v87
	s_waitcnt lgkmcnt(0)
	v_pk_add_f32 v[66:67], v[102:103], v[66:67]
	v_pk_fma_f32 v[62:63], v[98:99], v[62:63], v[94:95]
	v_cvt_pk_f16_f32 v88, v88, v89
	v_pk_add_f32 v[62:63], v[102:103], v[62:63]
	v_cvt_pk_f16_f32 v86, v92, v93
	v_cvt_pk_f16_f32 v92, v66, v67
	v_cvt_f32_f16_e32 v66, v68
	v_cvt_f32_f16_sdwa v67, v68 dst_sel:DWORD dst_unused:UNUSED_PAD src0_sel:WORD_1
	v_cvt_pk_f16_f32 v89, v62, v63
	v_cvt_f32_f16_e32 v62, v64
	v_cvt_f32_f16_sdwa v63, v64 dst_sel:DWORD dst_unused:UNUSED_PAD src0_sel:WORD_1
	v_pk_fma_f32 v[66:67], v[98:99], v[66:67], v[94:95]
	v_cvt_pk_f16_f32 v78, v106, v107
	v_pk_add_f32 v[66:67], v[102:103], v[66:67]
	v_pk_fma_f32 v[62:63], v[98:99], v[62:63], v[94:95]
	v_cvt_pk_f16_f32 v80, v66, v67
	v_pk_add_f32 v[62:63], v[102:103], v[62:63]
	v_cvt_f32_f16_e32 v66, v77
	v_cvt_f32_f16_sdwa v67, v77 dst_sel:DWORD dst_unused:UNUSED_PAD src0_sel:WORD_1
	v_cvt_pk_f16_f32 v77, v62, v63
	v_cvt_f32_f16_e32 v62, v81
	v_cvt_f32_f16_sdwa v63, v81 dst_sel:DWORD dst_unused:UNUSED_PAD src0_sel:WORD_1
	v_pk_fma_f32 v[66:67], v[100:101], v[66:67], v[96:97]
	s_waitcnt vmcnt(15)
	v_pk_fma_f16 v59, v83, v59, v88
	v_pk_add_f32 v[66:67], v[104:105], v[66:67]
	v_pk_fma_f32 v[62:63], v[100:101], v[62:63], v[96:97]
	v_cvt_pk_f16_f32 v95, v66, v67
	v_pk_add_f32 v[62:63], v[104:105], v[62:63]
	v_cvt_f32_f16_e32 v66, v69
	v_cvt_pk_f16_f32 v93, v62, v63
	v_cvt_f32_f16_e32 v62, v65
	v_cvt_f32_f16_sdwa v63, v65 dst_sel:DWORD dst_unused:UNUSED_PAD src0_sel:WORD_1
	v_cvt_f32_f16_sdwa v67, v69 dst_sel:DWORD dst_unused:UNUSED_PAD src0_sel:WORD_1
	v_pk_fma_f16 v61, v74, v61, v95
	v_pk_fma_f16 v58, v82, v58, v87
	v_pk_fma_f32 v[62:63], v[100:101], v[62:63], v[96:97]
	v_pk_fma_f32 v[64:65], v[100:101], v[66:67], v[96:97]
	v_pk_add_f32 v[62:63], v[104:105], v[62:63]
	v_pk_add_f32 v[64:65], v[104:105], v[64:65]
	v_cvt_pk_f16_f32 v81, v62, v63
	v_mov_b32_e32 v62, v0
	v_cvt_pk_f16_f32 v91, v64, v65
	v_add_u32_e32 v63, 0xffffff00, v62
	v_lshlrev_b32_e32 v62, 4, v62
	v_ashrrev_i32_e32 v94, 4, v63
	v_and_b32_e32 v90, 0xf0, v62
	v_pk_fma_f16 v60, v84, v60, v92
	s_waitcnt vmcnt(11)
	v_pk_fma_f16 v62, v82, v70, v87
	v_pk_fma_f16 v51, v83, v51, v86
	v_pk_fma_f16 v53, v74, v53, v93
	v_pk_fma_f16 v50, v82, v50, v85
	v_pk_fma_f16 v52, v84, v52, v89
	v_pk_fma_f16 v43, v83, v43, v79
	v_pk_fma_f16 v45, v74, v45, v91
	v_pk_fma_f16 v42, v82, v42, v78
	v_pk_fma_f16 v44, v84, v44, v80
	v_pk_fma_f16 v35, v83, v35, v76
	v_pk_fma_f16 v37, v74, v37, v81
	v_pk_fma_f16 v34, v82, v34, v75
	v_pk_fma_f16 v36, v84, v36, v77
	s_waitcnt vmcnt(8)
	v_pk_fma_f16 v38, v82, v38, v75
	v_pk_fma_f16 v63, v83, v71, v88
	v_pk_fma_f16 v65, v74, v73, v95
	v_pk_fma_f16 v64, v84, v72, v92
	v_pk_max_f16 v60, v60, 0
	v_pk_max_f16 v58, v58, 0
	v_pk_max_f16 v61, v61, 0
	v_pk_max_f16 v59, v59, 0
	v_pk_max_f16 v62, v62, 0
	v_mad_u64_u32 v[96:97], s[24:25], v94, s22, v[90:91]
	v_pk_fma_f16 v55, v83, v55, v86
	v_pk_fma_f16 v57, v74, v57, v93
	v_pk_fma_f16 v54, v82, v54, v85
	v_pk_fma_f16 v56, v84, v56, v89
	v_pk_max_f16 v52, v52, 0
	v_pk_max_f16 v50, v50, 0
	v_pk_max_f16 v53, v53, 0
	v_pk_max_f16 v51, v51, 0
	v_pk_fma_f16 v47, v83, v47, v79
	v_pk_fma_f16 v49, v74, v49, v91
	v_pk_fma_f16 v46, v82, v46, v78
	v_pk_fma_f16 v48, v84, v48, v80
	v_pk_max_f16 v44, v44, 0
	v_pk_max_f16 v42, v42, 0
	v_pk_max_f16 v45, v45, 0
	v_pk_max_f16 v43, v43, 0
	v_pk_fma_f16 v39, v83, v39, v76
	v_pk_fma_f16 v41, v74, v41, v81
	v_pk_fma_f16 v40, v84, v40, v77
	v_pk_max_f16 v36, v36, 0
	v_pk_max_f16 v34, v34, 0
	v_pk_max_f16 v37, v37, 0
	v_pk_max_f16 v35, v35, 0
	v_pk_max_f16 v38, v38, 0
	v_pk_max_f16 v64, v64, 0
	v_pk_max_f16 v65, v65, 0
	v_pk_max_f16 v63, v63, 0
	ds_write_b128 v96, v[58:61]
	ds_write_b128 v96, v[62:65] offset:17408
	v_pk_add_f16 v73, v58, v62
	v_pk_max_f16 v56, v56, 0
	v_pk_max_f16 v54, v54, 0
	v_pk_max_f16 v57, v57, 0
	v_pk_max_f16 v55, v55, 0
	ds_write_b128 v96, v[50:53] offset:4352
	ds_write_b128 v96, v[54:57] offset:21760
	v_pk_max_f16 v48, v48, 0
	v_pk_max_f16 v46, v46, 0
	v_pk_max_f16 v49, v49, 0
	v_pk_max_f16 v47, v47, 0
	ds_write_b128 v96, v[42:45] offset:8704
	ds_write_b128 v96, v[46:49] offset:26112
	v_pk_max_f16 v40, v40, 0
	v_pk_max_f16 v41, v41, 0
	v_pk_max_f16 v39, v39, 0
	ds_write_b128 v96, v[34:37] offset:13056
	ds_write_b128 v96, v[38:41] offset:30464
	s_waitcnt lgkmcnt(0)
	s_barrier
	v_pk_add_f16 v62, v34, v38
	v_add_u32_e32 v34, s21, v94
	v_lshl_or_b32 v38, v34, 8, v90
	v_pk_add_f16 v71, v60, v64
	v_pk_add_f16 v60, v35, v39
	v_add_u32_e32 v34, 0x1000, v38
	v_add_u32_e32 v39, 0x2000, v38
	v_pk_add_f16 v69, v61, v65
	v_pk_add_f16 v72, v59, v63
	v_pk_add_f16 v65, v53, v57
	v_pk_add_f16 v67, v52, v56
	v_pk_add_f16 v68, v51, v55
	v_pk_add_f16 v70, v50, v54
	v_pk_add_f16 v61, v45, v49
	v_pk_add_f16 v63, v44, v48
	v_pk_add_f16 v64, v43, v47
	v_pk_add_f16 v66, v42, v46
	v_pk_add_f16 v58, v37, v41
	v_pk_add_f16 v59, v36, v40
	buffer_load_dwordx4 v[100:103], v38, s[8:11], 0 offen sc1
	buffer_load_dwordx4 v[50:53], v34, s[8:11], 0 offen sc1
	v_add_u32_e32 v40, 0x3000, v38
	buffer_load_dwordx4 v[42:45], v39, s[8:11], 0 offen sc1
	buffer_load_dwordx4 v[34:37], v40, s[8:11], 0 offen sc1
	v_add_u32_e32 v39, 0x4000, v38
	v_add_u32_e32 v40, 0x5000, v38
	buffer_load_dwordx4 v[104:107], v39, s[8:11], 0 offen sc1
	buffer_load_dwordx4 v[54:57], v40, s[8:11], 0 offen sc1
	v_add_u32_e32 v90, 0x6000, v38
	v_add_u32_e32 v94, 0x7000, v38
	buffer_load_dwordx4 v[46:49], v90, s[8:11], 0 offen sc1
	buffer_load_dwordx4 v[38:41], v94, s[8:11], 0 offen sc1
	v_mov_b32_e32 v90, v0
	s_waitcnt vmcnt(15)
	v_pk_fma_f16 v27, v83, v27, v88
	v_add_u32_e32 v94, 0xffffff00, v90
	v_lshlrev_b32_e32 v90, 4, v90
	v_ashrrev_i32_e32 v109, 4, v94
	v_and_b32_e32 v108, 0xf0, v90
	v_pk_fma_f16 v29, v74, v29, v95
	v_pk_fma_f16 v26, v82, v26, v87
	v_pk_fma_f16 v28, v84, v28, v92
	s_waitcnt vmcnt(11)
	v_pk_fma_f16 v30, v82, v30, v87
	v_pk_fma_f16 v19, v83, v19, v86
	v_pk_fma_f16 v21, v74, v21, v93
	v_pk_fma_f16 v18, v82, v18, v85
	v_pk_fma_f16 v20, v84, v20, v89
	v_pk_fma_f16 v11, v83, v11, v79
	v_pk_fma_f16 v13, v74, v13, v91
	v_pk_fma_f16 v10, v82, v10, v78
	v_pk_fma_f16 v12, v84, v12, v80
	v_pk_fma_f16 v3, v83, v3, v76
	v_pk_fma_f16 v5, v74, v5, v81
	v_pk_fma_f16 v2, v82, v2, v75
	v_pk_fma_f16 v4, v84, v4, v77
	s_waitcnt vmcnt(8)
	v_pk_fma_f16 v6, v82, v6, v75
	v_pk_fma_f16 v31, v83, v31, v88
	v_pk_fma_f16 v33, v74, v33, v95
	v_pk_fma_f16 v32, v84, v32, v92
	v_pk_max_f16 v28, v28, 0
	v_pk_max_f16 v26, v26, 0
	v_pk_max_f16 v29, v29, 0
	v_pk_max_f16 v27, v27, 0
	v_pk_max_f16 v30, v30, 0
	v_mad_u64_u32 v[110:111], s[24:25], v109, s22, v[108:109]
	v_pk_fma_f16 v23, v83, v23, v86
	v_pk_fma_f16 v25, v74, v25, v93
	v_pk_fma_f16 v22, v82, v22, v85
	v_pk_fma_f16 v24, v84, v24, v89
	v_pk_max_f16 v20, v20, 0
	v_pk_max_f16 v18, v18, 0
	v_pk_max_f16 v21, v21, 0
	v_pk_max_f16 v19, v19, 0
	v_pk_fma_f16 v15, v83, v15, v79
	v_pk_fma_f16 v17, v74, v17, v91
	v_pk_fma_f16 v14, v82, v14, v78
	v_pk_fma_f16 v16, v84, v16, v80
	v_pk_max_f16 v12, v12, 0
	v_pk_max_f16 v10, v10, 0
	v_pk_max_f16 v13, v13, 0
	v_pk_max_f16 v11, v11, 0
	v_pk_fma_f16 v7, v83, v7, v76
	v_pk_fma_f16 v9, v74, v9, v81
	v_pk_fma_f16 v8, v84, v8, v77
	v_pk_max_f16 v4, v4, 0
	v_pk_max_f16 v2, v2, 0
	v_pk_max_f16 v5, v5, 0
	v_pk_max_f16 v3, v3, 0
	v_pk_max_f16 v6, v6, 0
	v_pk_max_f16 v32, v32, 0
	v_pk_max_f16 v33, v33, 0
	v_pk_max_f16 v31, v31, 0
	ds_write_b128 v110, v[26:29] offset:34816
	ds_write_b128 v110, v[30:33] offset:52224
	v_pk_add_f16 v129, v26, v30
	v_pk_max_f16 v24, v24, 0
	v_pk_max_f16 v22, v22, 0
	v_pk_max_f16 v25, v25, 0
	v_pk_max_f16 v23, v23, 0
	ds_write_b128 v110, v[18:21] offset:39168
	ds_write_b128 v110, v[22:25] offset:56576
	v_pk_max_f16 v16, v16, 0
	v_pk_max_f16 v14, v14, 0
	v_pk_max_f16 v17, v17, 0
	v_pk_max_f16 v15, v15, 0
	ds_write_b128 v110, v[10:13] offset:43520
	ds_write_b128 v110, v[14:17] offset:60928
	v_pk_max_f16 v8, v8, 0
	v_pk_max_f16 v9, v9, 0
	v_pk_max_f16 v7, v7, 0
	ds_write_b128 v110, v[2:5] offset:47872
	ds_write_b128 v110, v[6:9] offset:65280
	v_pk_add_f16 v30, v2, v6
	v_add_u32_e32 v2, s19, v109
	v_lshl_or_b32 v6, v2, 8, v108
	v_pk_add_f16 v99, v28, v32
	v_pk_add_f16 v128, v27, v31
	v_pk_add_f16 v27, v4, v8
	v_pk_add_f16 v28, v3, v7
	v_add_u32_e32 v2, 0x1000, v6
	v_add_u32_e32 v7, 0x2000, v6
	v_add_u32_e32 v8, 0x3000, v6
	v_pk_add_f16 v97, v29, v33
	v_pk_add_f16 v33, v21, v25
	v_pk_add_f16 v94, v20, v24
	v_pk_add_f16 v96, v19, v23
	v_pk_add_f16 v98, v18, v22
	v_pk_add_f16 v29, v13, v17
	v_pk_add_f16 v31, v12, v16
	v_pk_add_f16 v32, v11, v15
	v_pk_add_f16 v90, v10, v14
	v_pk_add_f16 v26, v5, v9
	buffer_load_dwordx4 v[108:111], v6, s[8:11], 0 offen sc1
	buffer_load_dwordx4 v[18:21], v2, s[8:11], 0 offen sc1
	buffer_load_dwordx4 v[10:13], v7, s[8:11], 0 offen sc1
	s_nop 0
	buffer_load_dwordx4 v[2:5], v8, s[8:11], 0 offen sc1
	v_add_u32_e32 v7, 0x4000, v6
	v_add_u32_e32 v8, 0x5000, v6
	v_add_u32_e32 v116, 0x6000, v6
	buffer_load_dwordx4 v[112:115], v7, s[8:11], 0 offen sc1
	buffer_load_dwordx4 v[22:25], v8, s[8:11], 0 offen sc1
	v_add_u32_e32 v117, 0x7000, v6
	buffer_load_dwordx4 v[14:17], v116, s[8:11], 0 offen sc1
	buffer_load_dwordx4 v[6:9], v117, s[8:11], 0 offen sc1
	v_fma_mix_f32 v192, v73, s44, 0 op_sel_hi:[1,0,0]
	v_fma_mix_f32 v193, v73, s44, 0 op_sel:[1,0,0] op_sel_hi:[1,0,0]
	v_fma_mix_f32 v192, v129, s44, v192 op_sel_hi:[1,0,0]
	v_fma_mix_f32 v193, v129, s44, v193 op_sel:[1,0,0] op_sel_hi:[1,0,0]
	v_fma_mix_f32 v194, v72, s44, 0 op_sel_hi:[1,0,0]
	v_fma_mix_f32 v195, v72, s44, 0 op_sel:[1,0,0] op_sel_hi:[1,0,0]
	v_fma_mix_f32 v194, v128, s44, v194 op_sel_hi:[1,0,0]
	v_fma_mix_f32 v195, v128, s44, v195 op_sel:[1,0,0] op_sel_hi:[1,0,0]
	v_fma_mix_f32 v196, v71, s44, 0 op_sel_hi:[1,0,0]
	v_fma_mix_f32 v197, v71, s44, 0 op_sel:[1,0,0] op_sel_hi:[1,0,0]
	v_fma_mix_f32 v196, v99, s44, v196 op_sel_hi:[1,0,0]
	v_fma_mix_f32 v197, v99, s44, v197 op_sel:[1,0,0] op_sel_hi:[1,0,0]
	v_fma_mix_f32 v198, v69, s44, 0 op_sel_hi:[1,0,0]
	v_fma_mix_f32 v199, v69, s44, 0 op_sel:[1,0,0] op_sel_hi:[1,0,0]
	v_fma_mix_f32 v198, v97, s44, v198 op_sel_hi:[1,0,0]
	v_fma_mix_f32 v199, v97, s44, v199 op_sel:[1,0,0] op_sel_hi:[1,0,0]
	v_fma_mix_f32 v200, v70, s44, 0 op_sel_hi:[1,0,0]
	v_fma_mix_f32 v201, v70, s44, 0 op_sel:[1,0,0] op_sel_hi:[1,0,0]
	v_fma_mix_f32 v200, v98, s44, v200 op_sel_hi:[1,0,0]
	v_fma_mix_f32 v201, v98, s44, v201 op_sel:[1,0,0] op_sel_hi:[1,0,0]
	v_fma_mix_f32 v202, v68, s44, 0 op_sel_hi:[1,0,0]
	v_fma_mix_f32 v203, v68, s44, 0 op_sel:[1,0,0] op_sel_hi:[1,0,0]
	v_fma_mix_f32 v202, v96, s44, v202 op_sel_hi:[1,0,0]
	v_fma_mix_f32 v203, v96, s44, v203 op_sel:[1,0,0] op_sel_hi:[1,0,0]
	v_fma_mix_f32 v204, v67, s44, 0 op_sel_hi:[1,0,0]
	v_fma_mix_f32 v205, v67, s44, 0 op_sel:[1,0,0] op_sel_hi:[1,0,0]
	v_fma_mix_f32 v204, v94, s44, v204 op_sel_hi:[1,0,0]
	v_fma_mix_f32 v205, v94, s44, v205 op_sel:[1,0,0] op_sel_hi:[1,0,0]
	v_fma_mix_f32 v206, v65, s44, 0 op_sel_hi:[1,0,0]
	v_fma_mix_f32 v207, v65, s44, 0 op_sel:[1,0,0] op_sel_hi:[1,0,0]
	v_fma_mix_f32 v206, v33, s44, v206 op_sel_hi:[1,0,0]
	v_fma_mix_f32 v207, v33, s44, v207 op_sel:[1,0,0] op_sel_hi:[1,0,0]
	v_fma_mix_f32 v208, v66, s44, 0 op_sel_hi:[1,0,0]
	v_fma_mix_f32 v209, v66, s44, 0 op_sel:[1,0,0] op_sel_hi:[1,0,0]
	v_fma_mix_f32 v208, v90, s44, v208 op_sel_hi:[1,0,0]
	v_fma_mix_f32 v209, v90, s44, v209 op_sel:[1,0,0] op_sel_hi:[1,0,0]
	v_fma_mix_f32 v210, v64, s44, 0 op_sel_hi:[1,0,0]
	v_fma_mix_f32 v211, v64, s44, 0 op_sel:[1,0,0] op_sel_hi:[1,0,0]
	v_fma_mix_f32 v210, v32, s44, v210 op_sel_hi:[1,0,0]
	v_fma_mix_f32 v211, v32, s44, v211 op_sel:[1,0,0] op_sel_hi:[1,0,0]
	v_fma_mix_f32 v212, v63, s44, 0 op_sel_hi:[1,0,0]
	v_fma_mix_f32 v213, v63, s44, 0 op_sel:[1,0,0] op_sel_hi:[1,0,0]
	v_fma_mix_f32 v212, v31, s44, v212 op_sel_hi:[1,0,0]
	v_fma_mix_f32 v213, v31, s44, v213 op_sel:[1,0,0] op_sel_hi:[1,0,0]
	v_fma_mix_f32 v214, v61, s44, 0 op_sel_hi:[1,0,0]
	v_fma_mix_f32 v215, v61, s44, 0 op_sel:[1,0,0] op_sel_hi:[1,0,0]
	v_fma_mix_f32 v214, v29, s44, v214 op_sel_hi:[1,0,0]
	v_fma_mix_f32 v215, v29, s44, v215 op_sel:[1,0,0] op_sel_hi:[1,0,0]
	v_fma_mix_f32 v216, v62, s44, 0 op_sel_hi:[1,0,0]
	v_fma_mix_f32 v217, v62, s44, 0 op_sel:[1,0,0] op_sel_hi:[1,0,0]
	v_fma_mix_f32 v216, v30, s44, v216 op_sel_hi:[1,0,0]
	v_fma_mix_f32 v217, v30, s44, v217 op_sel:[1,0,0] op_sel_hi:[1,0,0]
	v_fma_mix_f32 v218, v60, s44, 0 op_sel_hi:[1,0,0]
	v_fma_mix_f32 v219, v60, s44, 0 op_sel:[1,0,0] op_sel_hi:[1,0,0]
	v_fma_mix_f32 v218, v28, s44, v218 op_sel_hi:[1,0,0]
	v_fma_mix_f32 v219, v28, s44, v219 op_sel:[1,0,0] op_sel_hi:[1,0,0]
	v_fma_mix_f32 v220, v59, s44, 0 op_sel_hi:[1,0,0]
	v_fma_mix_f32 v221, v59, s44, 0 op_sel:[1,0,0] op_sel_hi:[1,0,0]
	v_fma_mix_f32 v220, v27, s44, v220 op_sel_hi:[1,0,0]
	v_fma_mix_f32 v221, v27, s44, v221 op_sel:[1,0,0] op_sel_hi:[1,0,0]
	v_fma_mix_f32 v222, v58, s44, 0 op_sel_hi:[1,0,0]
	v_fma_mix_f32 v223, v58, s44, 0 op_sel:[1,0,0] op_sel_hi:[1,0,0]
	v_fma_mix_f32 v222, v26, s44, v222 op_sel_hi:[1,0,0]
	v_fma_mix_f32 v223, v26, s44, v223 op_sel:[1,0,0] op_sel_hi:[1,0,0]
	s_waitcnt lgkmcnt(0)
	s_barrier
	s_lshl_b32 s8, s12, 16
	v_add_u32_e32 v116, 0xffffff00, v130
	v_lshlrev_b32_e32 v117, 3, v130
	v_lshrrev_b32_e32 v131, 4, v116
	v_and_b32_e32 v117, 56, v117
	v_lshrrev_b32_e32 v125, 3, v116
	v_ashrrev_i32_e32 v116, 3, v116
	s_movk_i32 s10, 0xffc0
	s_or_b32 s8, s8, s18
	v_lshl_or_b32 v124, v117, 1, v132
	v_bfi_b32 v121, s10, v116, v125
	s_movk_i32 s11, 0x90
	v_or_b32_e32 v120, s8, v117
	v_mad_u64_u32 v[116:117], s[8:9], v121, s11, v[124:125]
	ds_read_b128 v[116:119], v116
	v_lshlrev_b32_e32 v133, 1, v120
	v_lshrrev_b32_e32 v127, 3, v130
	v_ashrrev_i32_e32 v120, 3, v130
	v_bfi_b32 v134, s10, v120, v127
	v_lshl_add_u32 v126, v121, 8, v133
	v_mad_u64_u32 v[120:121], s[8:9], v134, s11, v[124:125]
	ds_read_b128 v[120:123], v120
	s_waitcnt lgkmcnt(1)
	buffer_store_dwordx4 v[116:119], v126, s[4:7], 0 offen sc1
	v_lshl_add_u32 v134, v134, 8, v133
	s_waitcnt vmcnt(16)
	v_pk_fma_f16 v100, v82, v100, v87
	v_add_u32_e32 v116, 0x100, v130
	v_ashrrev_i32_e32 v116, 3, v116
	v_bfi_b32 v135, s10, v116, v125
	v_mad_u64_u32 v[116:117], s[8:9], v135, s11, v[124:125]
	v_add_u32_e32 v125, 0x200, v130
	v_ashrrev_i32_e32 v125, 3, v125
	v_bfi_b32 v136, s10, v125, v127
	ds_read_b128 v[116:119], v116
	v_mad_u64_u32 v[124:125], s[8:9], v136, s11, v[124:125]
	ds_read_b128 v[124:127], v124
	s_waitcnt lgkmcnt(2)
	buffer_store_dwordx4 v[120:123], v134, s[4:7], 0 offen sc1
	v_pk_fma_f16 v101, v83, v101, v88
	v_pk_fma_f16 v102, v84, v102, v92
	v_lshl_add_u32 v120, v135, 8, v133
	s_waitcnt lgkmcnt(1)
	buffer_store_dwordx4 v[116:119], v120, s[4:7], 0 offen sc1
	v_pk_fma_f16 v103, v74, v103, v95
	s_waitcnt vmcnt(17)
	v_pk_fma_f16 v50, v82, v50, v85
	v_lshl_add_u32 v116, v136, 8, v133
	s_waitcnt lgkmcnt(0)
	buffer_store_dwordx4 v[124:127], v116, s[4:7], 0 offen sc1
	v_lshlrev_b32_e32 v116, 4, v130
	v_and_b32_e32 v116, 0xf0, v116
	v_pk_fma_f16 v51, v83, v51, v86
	v_pk_fma_f16 v52, v84, v52, v89
	v_pk_fma_f16 v53, v74, v53, v93
	s_waitcnt vmcnt(14)
	v_pk_fma_f16 v56, v84, v56, v89
	v_pk_fma_f16 v57, v74, v57, v93
	v_pk_fma_f16 v42, v82, v42, v78
	v_pk_fma_f16 v43, v83, v43, v79
	v_pk_fma_f16 v44, v84, v44, v80
	v_pk_fma_f16 v45, v74, v45, v91
	s_waitcnt vmcnt(13)
	v_pk_fma_f16 v46, v82, v46, v78
	v_pk_fma_f16 v47, v83, v47, v79
	v_pk_fma_f16 v104, v82, v104, v87
	v_pk_fma_f16 v105, v83, v105, v88
	v_pk_fma_f16 v106, v84, v106, v92
	v_pk_fma_f16 v107, v74, v107, v95
	v_pk_max_f16 v103, v103, 0
	v_pk_max_f16 v102, v102, 0
	v_pk_max_f16 v101, v101, 0
	v_pk_max_f16 v100, v100, 0
	v_mad_u64_u32 v[116:117], s[8:9], v131, s22, v[116:117]
	v_pk_fma_f16 v54, v82, v54, v85
	v_pk_fma_f16 v55, v83, v55, v86
	v_pk_max_f16 v53, v53, 0
	v_pk_max_f16 v52, v52, 0
	v_pk_max_f16 v51, v51, 0
	v_pk_max_f16 v50, v50, 0
	v_pk_max_f16 v57, v57, 0
	v_pk_max_f16 v56, v56, 0
	v_pk_fma_f16 v48, v84, v48, v80
	v_pk_fma_f16 v49, v74, v49, v91
	v_pk_max_f16 v45, v45, 0
	v_pk_max_f16 v44, v44, 0
	v_pk_max_f16 v43, v43, 0
	v_pk_max_f16 v42, v42, 0
	v_pk_max_f16 v47, v47, 0
	v_pk_max_f16 v46, v46, 0
	v_pk_max_f16 v107, v107, 0
	v_pk_max_f16 v106, v106, 0
	v_pk_max_f16 v105, v105, 0
	v_pk_max_f16 v104, v104, 0
	ds_write_b128 v116, v[100:103]
	ds_write_b128 v116, v[104:107] offset:17408
	v_pk_max_f16 v55, v55, 0
	v_pk_max_f16 v54, v54, 0
	ds_write_b128 v116, v[50:53] offset:4352
	ds_write_b128 v116, v[54:57] offset:21760
	v_pk_add_f16 v53, v53, v57
	v_pk_add_f16 v52, v52, v56
	v_pk_max_f16 v49, v49, 0
	v_pk_max_f16 v48, v48, 0
	ds_write_b128 v116, v[42:45] offset:8704
	ds_write_b128 v116, v[46:49] offset:26112
	v_pk_add_f16 v56, v43, v47
	v_pk_add_f16 v57, v42, v46
	v_pk_fma_f16 v34, v82, v34, v75
	v_pk_fma_f16 v35, v83, v35, v76
	v_pk_fma_f16 v36, v84, v36, v77
	v_pk_fma_f16 v37, v74, v37, v81
	s_waitcnt vmcnt(12)
	v_pk_fma_f16 v42, v82, v38, v75
	v_pk_fma_f16 v43, v83, v39, v76
	v_pk_add_f16 v100, v100, v104
	v_pk_add_f16 v51, v51, v55
	v_pk_add_f16 v50, v50, v54
	v_pk_add_f16 v54, v45, v49
	v_pk_add_f16 v55, v44, v48
	v_pk_fma_f16 v44, v84, v40, v77
	v_pk_fma_f16 v45, v74, v41, v81
	v_pk_max_f16 v41, v37, 0
	v_pk_max_f16 v40, v36, 0
	v_pk_max_f16 v39, v35, 0
	v_pk_max_f16 v38, v34, 0
	v_pk_max_f16 v43, v43, 0
	v_pk_max_f16 v42, v42, 0
	v_mov_b32_e32 v104, v0
	v_pk_max_f16 v45, v45, 0
	v_pk_max_f16 v44, v44, 0
	ds_write_b128 v116, v[38:41] offset:13056
	ds_write_b128 v116, v[42:45] offset:30464
	v_pk_add_f16 v36, v39, v43
	v_pk_add_f16 v37, v38, v42
	s_waitcnt lgkmcnt(0)
	s_barrier
	v_pk_add_f16 v101, v101, v105
	v_add_u32_e32 v38, 0xffffff00, v104
	v_lshlrev_b32_e32 v39, 3, v104
	v_lshrrev_b32_e32 v105, 4, v38
	v_and_b32_e32 v39, 56, v39
	v_lshrrev_b32_e32 v47, 3, v38
	v_ashrrev_i32_e32 v38, 3, v38
	v_lshl_or_b32 v46, v39, 1, v132
	v_bfi_b32 v43, s10, v38, v47
	v_or_b32_e32 v42, s2, v39
	v_mad_u64_u32 v[38:39], s[8:9], v43, s11, v[46:47]
	v_pk_add_f16 v34, v41, v45
	v_pk_add_f16 v35, v40, v44
	ds_read_b128 v[38:41], v38 offset:18432
	v_pk_add_f16 v102, v102, v106
	v_lshlrev_b32_e32 v106, 1, v42
	v_lshrrev_b32_e32 v49, 3, v104
	v_ashrrev_i32_e32 v42, 3, v104
	v_pk_add_f16 v103, v103, v107
	v_bfi_b32 v107, s10, v42, v49
	v_lshl_add_u32 v48, v43, 8, v106
	v_mad_u64_u32 v[42:43], s[8:9], v107, s11, v[46:47]
	ds_read_b128 v[42:45], v42 offset:18432
	s_waitcnt lgkmcnt(1)
	buffer_store_dwordx4 v[38:41], v48, s[4:7], 0 offen sc1
	v_lshl_add_u32 v107, v107, 8, v106
	s_waitcnt vmcnt(11)
	v_pk_fma_f16 v18, v82, v18, v85
	v_add_u32_e32 v38, 0x100, v104
	v_ashrrev_i32_e32 v38, 3, v38
	v_bfi_b32 v116, s10, v38, v47
	v_mad_u64_u32 v[38:39], s[8:9], v116, s11, v[46:47]
	v_add_u32_e32 v47, 0x200, v104
	v_ashrrev_i32_e32 v47, 3, v47
	v_bfi_b32 v117, s10, v47, v49
	ds_read_b128 v[38:41], v38 offset:18432
	v_mad_u64_u32 v[46:47], s[8:9], v117, s11, v[46:47]
	ds_read_b128 v[46:49], v46 offset:18432
	s_waitcnt lgkmcnt(2)
	buffer_store_dwordx4 v[42:45], v107, s[4:7], 0 offen sc1
	v_pk_fma_f16 v19, v83, v19, v86
	v_pk_fma_f16 v20, v84, v20, v89
	v_lshl_add_u32 v42, v116, 8, v106
	s_waitcnt lgkmcnt(1)
	buffer_store_dwordx4 v[38:41], v42, s[4:7], 0 offen sc1
	v_pk_fma_f16 v21, v74, v21, v93
	s_waitcnt vmcnt(9)
	v_pk_fma_f16 v24, v84, v24, v89
	v_lshl_add_u32 v38, v117, 8, v106
	s_waitcnt lgkmcnt(0)
	buffer_store_dwordx4 v[46:49], v38, s[4:7], 0 offen sc1
	v_lshlrev_b32_e32 v38, 4, v104
	v_pk_fma_f16 v39, v83, v109, v88
	v_and_b32_e32 v46, 0xf0, v38
	v_pk_fma_f16 v38, v82, v108, v87
	v_pk_fma_f16 v40, v84, v110, v92
	v_pk_fma_f16 v41, v74, v111, v95
	v_pk_fma_f16 v25, v74, v25, v93
	v_pk_fma_f16 v10, v82, v10, v78
	v_pk_fma_f16 v11, v83, v11, v79
	v_pk_fma_f16 v12, v84, v12, v80
	v_pk_fma_f16 v13, v74, v13, v91
	v_pk_fma_f16 v2, v82, v2, v75
	v_pk_fma_f16 v3, v83, v3, v76
	v_pk_fma_f16 v4, v84, v4, v77
	v_pk_fma_f16 v5, v74, v5, v81
	s_waitcnt vmcnt(8)
	v_pk_fma_f16 v6, v82, v6, v75
	v_pk_fma_f16 v7, v83, v7, v76
	v_pk_fma_f16 v42, v82, v112, v87
	v_pk_fma_f16 v43, v83, v113, v88
	v_pk_fma_f16 v44, v84, v114, v92
	v_pk_fma_f16 v45, v74, v115, v95
	v_pk_max_f16 v41, v41, 0
	v_pk_max_f16 v40, v40, 0
	v_pk_max_f16 v39, v39, 0
	v_pk_max_f16 v38, v38, 0
	v_mad_u64_u32 v[46:47], s[8:9], v105, s22, v[46:47]
	v_pk_fma_f16 v22, v82, v22, v85
	v_pk_fma_f16 v23, v83, v23, v86
	v_pk_max_f16 v21, v21, 0
	v_pk_max_f16 v20, v20, 0
	v_pk_max_f16 v19, v19, 0
	v_pk_max_f16 v18, v18, 0
	v_pk_max_f16 v25, v25, 0
	v_pk_max_f16 v24, v24, 0
	v_pk_fma_f16 v14, v82, v14, v78
	v_pk_fma_f16 v15, v83, v15, v79
	v_pk_fma_f16 v16, v84, v16, v80
	v_pk_fma_f16 v17, v74, v17, v91
	v_pk_max_f16 v13, v13, 0
	v_pk_max_f16 v12, v12, 0
	v_pk_max_f16 v11, v11, 0
	v_pk_max_f16 v10, v10, 0
	v_pk_fma_f16 v8, v84, v8, v77
	v_pk_fma_f16 v9, v74, v9, v81
	v_pk_max_f16 v5, v5, 0
	v_pk_max_f16 v4, v4, 0
	v_pk_max_f16 v3, v3, 0
	v_pk_max_f16 v2, v2, 0
	v_pk_max_f16 v7, v7, 0
	v_pk_max_f16 v6, v6, 0
	v_pk_max_f16 v45, v45, 0
	v_pk_max_f16 v44, v44, 0
	v_pk_max_f16 v43, v43, 0
	v_pk_max_f16 v42, v42, 0
	ds_write_b128 v46, v[38:41] offset:34816
	ds_write_b128 v46, v[42:45] offset:52224
	v_pk_max_f16 v23, v23, 0
	v_pk_max_f16 v22, v22, 0
	ds_write_b128 v46, v[18:21] offset:39168
	ds_write_b128 v46, v[22:25] offset:56576
	v_pk_add_f16 v21, v21, v25
	v_pk_add_f16 v20, v20, v24
	v_pk_max_f16 v17, v17, 0
	v_pk_max_f16 v16, v16, 0
	v_pk_max_f16 v15, v15, 0
	v_pk_max_f16 v14, v14, 0
	ds_write_b128 v46, v[10:13] offset:43520
	ds_write_b128 v46, v[14:17] offset:60928
	v_pk_max_f16 v9, v9, 0
	v_pk_max_f16 v8, v8, 0
	ds_write_b128 v46, v[2:5] offset:47872
	ds_write_b128 v46, v[6:9] offset:65280
	v_pk_add_f16 v24, v3, v7
	v_pk_add_f16 v25, v2, v6
	v_pk_add_f16 v19, v19, v23
	v_pk_add_f16 v18, v18, v22
	v_pk_add_f16 v22, v5, v9
	v_pk_add_f16 v23, v4, v8
	v_pk_add_f16 v38, v38, v42
	v_fma_mix_f32 v192, v100, s44, v192 op_sel_hi:[1,0,0]
	v_fma_mix_f32 v193, v100, s44, v193 op_sel:[1,0,0] op_sel_hi:[1,0,0]
	v_fma_mixlo_f16 v224, v38, s44, v192 op_sel_hi:[1,0,0]
	v_pk_add_f16 v39, v39, v43
	v_fma_mixhi_f16 v224, v38, s44, v193 op_sel:[1,0,0] op_sel_hi:[1,0,0]
	v_fma_mix_f32 v194, v101, s44, v194 op_sel_hi:[1,0,0]
	v_fma_mix_f32 v195, v101, s44, v195 op_sel:[1,0,0] op_sel_hi:[1,0,0]
	v_pk_add_f16 v15, v11, v15
	v_pk_add_f16 v14, v10, v14
	v_fma_mixlo_f16 v225, v39, s44, v194 op_sel_hi:[1,0,0]
	s_nop 0
	v_fma_mixhi_f16 v225, v39, s44, v195 op_sel:[1,0,0] op_sel_hi:[1,0,0]
	s_mov_b32 s2, 0x3e000000
	v_pk_add_f16 v40, v40, v44
	v_fma_mix_f32 v196, v102, s44, v196 op_sel_hi:[1,0,0]
	v_fma_mix_f32 v197, v102, s44, v197 op_sel:[1,0,0] op_sel_hi:[1,0,0]
	v_fma_mixlo_f16 v226, v40, s44, v196 op_sel_hi:[1,0,0]
	v_pk_add_f16 v41, v41, v45
	v_fma_mixhi_f16 v226, v40, s44, v197 op_sel:[1,0,0] op_sel_hi:[1,0,0]
	v_fma_mix_f32 v198, v103, s44, v198 op_sel_hi:[1,0,0]
	v_fma_mix_f32 v199, v103, s44, v199 op_sel:[1,0,0] op_sel_hi:[1,0,0]
	v_pk_add_f16 v17, v13, v17
	v_pk_add_f16 v16, v12, v16
	v_fma_mixlo_f16 v227, v41, s44, v198 op_sel_hi:[1,0,0]
	v_add_u32_e32 v38, 0x1a000, v46
	v_fma_mixhi_f16 v227, v41, s44, v199 op_sel:[1,0,0] op_sel_hi:[1,0,0]
	v_fma_mix_f32 v200, v18, s44, v200 op_sel_hi:[1,0,0]
	v_fma_mix_f32 v201, v18, s44, v201 op_sel:[1,0,0] op_sel_hi:[1,0,0]
	ds_write_b128 v38, v[224:227]
	v_fma_mixlo_f16 v228, v50, s44, v200 op_sel_hi:[1,0,0]
	v_fma_mix_f32 v202, v19, s44, v202 op_sel_hi:[1,0,0]
	v_fma_mixhi_f16 v228, v50, s44, v201 op_sel:[1,0,0] op_sel_hi:[1,0,0]
	s_nop 0
	v_fma_mixlo_f16 v229, v51, s44, v202 op_sel_hi:[1,0,0]
	v_fma_mix_f32 v203, v51, s44, v203 op_sel:[1,0,0] op_sel_hi:[1,0,0]
	v_fma_mixhi_f16 v229, v19, s44, v203 op_sel:[1,0,0] op_sel_hi:[1,0,0]
	v_fma_mix_f32 v204, v52, s44, v204 op_sel_hi:[1,0,0]
	v_fma_mix_f32 v205, v52, s44, v205 op_sel:[1,0,0] op_sel_hi:[1,0,0]
	v_fma_mixlo_f16 v230, v20, s44, v204 op_sel_hi:[1,0,0]
	v_fma_mix_f32 v206, v21, s44, v206 op_sel_hi:[1,0,0]
	v_fma_mixhi_f16 v230, v20, s44, v205 op_sel:[1,0,0] op_sel_hi:[1,0,0]
	s_nop 0
	v_fma_mixlo_f16 v231, v53, s44, v206 op_sel_hi:[1,0,0]
	v_fma_mix_f32 v207, v53, s44, v207 op_sel:[1,0,0] op_sel_hi:[1,0,0]
	v_fma_mixhi_f16 v231, v21, s44, v207 op_sel:[1,0,0] op_sel_hi:[1,0,0]
	v_fma_mix_f32 v208, v14, s44, v208 op_sel_hi:[1,0,0]
	v_fma_mix_f32 v209, v14, s44, v209 op_sel:[1,0,0] op_sel_hi:[1,0,0]
	v_fma_mix_f32 v210, v15, s44, v210 op_sel_hi:[1,0,0]
	ds_write_b128 v38, v[228:231] offset:4352
	v_fma_mixlo_f16 v232, v57, s44, v208 op_sel_hi:[1,0,0]
	s_nop 0
	v_fma_mixhi_f16 v232, v57, s44, v209 op_sel:[1,0,0] op_sel_hi:[1,0,0]
	v_fma_mix_f32 v211, v15, s44, v211 op_sel:[1,0,0] op_sel_hi:[1,0,0]
	v_fma_mixlo_f16 v233, v56, s44, v210 op_sel_hi:[1,0,0]
	s_nop 0
	v_fma_mixhi_f16 v233, v56, s44, v211 op_sel:[1,0,0] op_sel_hi:[1,0,0]
	v_fma_mix_f32 v212, v55, s44, v212 op_sel_hi:[1,0,0]
	v_fma_mix_f32 v213, v55, s44, v213 op_sel:[1,0,0] op_sel_hi:[1,0,0]
	v_fma_mixlo_f16 v234, v16, s44, v212 op_sel_hi:[1,0,0]
	v_fma_mix_f32 v214, v17, s44, v214 op_sel_hi:[1,0,0]
	v_fma_mixhi_f16 v234, v16, s44, v213 op_sel:[1,0,0] op_sel_hi:[1,0,0]
	s_nop 0
	v_fma_mixlo_f16 v235, v54, s44, v214 op_sel_hi:[1,0,0]
	v_fma_mix_f32 v215, v54, s44, v215 op_sel:[1,0,0] op_sel_hi:[1,0,0]
	v_fma_mixhi_f16 v235, v17, s44, v215 op_sel:[1,0,0] op_sel_hi:[1,0,0]
	v_fma_mix_f32 v216, v25, s44, v216 op_sel_hi:[1,0,0]
	v_fma_mix_f32 v217, v25, s44, v217 op_sel:[1,0,0] op_sel_hi:[1,0,0]
	v_fma_mix_f32 v218, v24, s44, v218 op_sel_hi:[1,0,0]
	ds_write_b128 v38, v[232:235] offset:8704
	v_fma_mixlo_f16 v236, v37, s44, v216 op_sel_hi:[1,0,0]
	s_nop 0
	v_fma_mixhi_f16 v236, v37, s44, v217 op_sel:[1,0,0] op_sel_hi:[1,0,0]
	v_fma_mix_f32 v219, v24, s44, v219 op_sel:[1,0,0] op_sel_hi:[1,0,0]
	v_fma_mixlo_f16 v237, v36, s44, v218 op_sel_hi:[1,0,0]
	s_nop 0
	v_fma_mixhi_f16 v237, v36, s44, v219 op_sel:[1,0,0] op_sel_hi:[1,0,0]
	v_fma_mix_f32 v220, v35, s44, v220 op_sel_hi:[1,0,0]
	v_fma_mix_f32 v221, v35, s44, v221 op_sel:[1,0,0] op_sel_hi:[1,0,0]
	v_fma_mixlo_f16 v238, v23, s44, v220 op_sel_hi:[1,0,0]
	v_fma_mix_f32 v222, v22, s44, v222 op_sel_hi:[1,0,0]
	v_fma_mixhi_f16 v238, v23, s44, v221 op_sel:[1,0,0] op_sel_hi:[1,0,0]
	s_nop 0
	v_fma_mixlo_f16 v239, v34, s44, v222 op_sel_hi:[1,0,0]
	v_fma_mix_f32 v223, v34, s44, v223 op_sel:[1,0,0] op_sel_hi:[1,0,0]
	v_fma_mixhi_f16 v239, v22, s44, v223 op_sel:[1,0,0] op_sel_hi:[1,0,0]
	s_cmpk_lt_u32 s15, 0x180
	s_cselect_b64 s[8:9], -1, 0
	s_cmpk_gt_u32 s15, 0x17f
	ds_write_b128 v38, v[236:239] offset:13056
	s_cbranch_scc1 .LBB3_3
	s_load_dwordx2 s[10:11], s[0:1], 0x78
	s_load_dwordx4 s[24:27], s[0:1], 0x50
	v_mov_b32_e32 v2, v0
	s_lshl_b64 s[22:23], s[12:13], 12
	s_waitcnt lgkmcnt(0)
	s_add_u32 s10, s10, s22
	v_lshlrev_b32_e32 v2, 3, v2
	s_addc_u32 s11, s11, s23
	v_and_b32_e32 v2, 0x1f8, v2
	global_load_dwordx2 v[136:137], v2, s[10:11]
	global_load_dwordx2 v[132:133], v2, s[10:11] offset:512
	global_load_dwordx2 v[128:129], v2, s[10:11] offset:1024
	global_load_dwordx2 v[124:125], v2, s[10:11] offset:1536
	global_load_dwordx2 v[134:135], v2, s[10:11] offset:2048
	global_load_dwordx2 v[130:131], v2, s[10:11] offset:2560
	global_load_dwordx2 v[126:127], v2, s[10:11] offset:3072
	global_load_dwordx2 v[122:123], v2, s[10:11] offset:3584
	s_lshl_b32 s2, s14, 4
	s_lshl_b32 s10, s17, 3
	s_add_i32 s10, s10, s2
	s_sub_i32 s2, s10, 32
	s_lshl_b64 s[2:3], s[2:3], 10
	v_lshl_or_b32 v2, v2, 1, s2
	v_mov_b32_e32 v3, s3
	v_lshl_add_u64 v[4:5], s[24:25], 0, v[2:3]
	global_load_dwordx4 v[18:21], v[4:5], off
	global_load_dwordx4 v[102:105], v[4:5], off offset:1024
	global_load_dwordx4 v[94:97], v[4:5], off offset:2048
	global_load_dwordx4 v[86:89], v[4:5], off offset:3072
	v_add_co_u32_e32 v4, vcc, s20, v4
	v_lshl_add_u64 v[6:7], s[26:27], 0, v[2:3]
	s_nop 0
	v_addc_co_u32_e32 v5, vcc, 0, v5, vcc
	global_load_dwordx4 v[78:81], v[4:5], off
	global_load_dwordx4 v[74:77], v[4:5], off offset:1024
	global_load_dwordx4 v[70:73], v[4:5], off offset:2048
	global_load_dwordx4 v[66:69], v[4:5], off offset:3072
	s_nop 0
	global_load_dwordx4 v[2:5], v[6:7], off
	global_load_dwordx4 v[118:121], v[6:7], off offset:1024
	global_load_dwordx4 v[114:117], v[6:7], off offset:2048
	global_load_dwordx4 v[110:113], v[6:7], off offset:3072
	v_add_co_u32_e32 v6, vcc, s20, v6
	s_nop 1
	v_addc_co_u32_e32 v7, vcc, 0, v7, vcc
	global_load_dwordx4 v[106:109], v[6:7], off
	global_load_dwordx4 v[98:101], v[6:7], off offset:1024
	global_load_dwordx4 v[90:93], v[6:7], off offset:2048
	global_load_dwordx4 v[82:85], v[6:7], off offset:3072
	s_branch .LBB3_4
